# long-segment (>64) handling: scalar length guards in K3 count and split sections; K2 out-degree overflow handled by ballot fast path instead of serial 52-step loop
# speedup vs baseline: 1.0323x; 1.0158x over previous
.LBB1_42:
	s_or_b64 exec, exec, s[10:11]
	s_load_dwordx2 s[28:29], s[0:1], 0x28
	s_waitcnt lgkmcnt(0)
	s_barrier
	s_and_saveexec_b64 s[0:1], vcc
	s_cbranch_execz .LBB1_45
	v_mov_b32_e32 v131, 0x18b40
	v_lshl_add_u32 v131, v0, 2, v131
	ds_read_b32 v131, v131
	s_waitcnt lgkmcnt(0)
	v_cmp_lt_u32_e32 vcc, 0x80, v131
	s_and_b64 exec, exec, vcc
	v_mov_b32_e32 v131, 1
	v_mov_b32_e32 v132, 0x19440
	ds_write_b32 v132, v131
.LBB1_45:
	s_or_b64 exec, exec, s[0:1]
	v_lshlrev_b32_e32 v130, 2, v130
	v_mov_b32_e32 v131, 0
	v_lshlrev_b32_e32 v134, 2, v164
	v_lshl_add_u64 v[162:163], s[8:9], 0, v[130:131]
	v_mov_b32_e32 v183, v1
	v_or_b32_e32 v169, 0x18fc0, v134
	v_add_u32_e32 v130, 0x18fd4, v134
	v_add_u32_e32 v135, 0x18b68, v134
	v_add_u32_e32 v136, 0x18ffc, v134
	v_add_u32_e32 v137, 0x18b7c, v134
	v_or_b32_e32 v170, 0x18b40, v134
	v_add_u32_e32 v132, 0x18b54, v134
	v_add_u32_e32 v133, 0x18fe8, v134
	ds_read_b32 v138, v169
	ds_read_b32 v139, v170
	ds_read_b32 v140, v130
	ds_read_b32 v141, v132
	ds_read_b32 v142, v133
	ds_read_b32 v135, v135
	ds_read_b32 v136, v136
	ds_read_b32 v137, v137
	s_waitcnt lgkmcnt(7)
	v_add_u32_e32 v130, v138, v1
	s_waitcnt lgkmcnt(6)
	v_cmp_lt_u32_e64 s[18:19], v1, v139
	s_waitcnt lgkmcnt(4)
	v_cmp_lt_u32_e32 vcc, v1, v141
	s_waitcnt lgkmcnt(2)
	v_cmp_lt_u32_e64 s[8:9], v1, v135
	v_cndmask_b32_e64 v130, 0, v130, s[18:19]
	v_lshl_add_u64 v[132:133], v[130:131], 1, s[26:27]
	v_add_u32_e32 v130, v140, v1
	v_cndmask_b32_e32 v130, 0, v130, vcc
	global_load_ushort v181, v[132:133], off
	v_lshl_add_u64 v[132:133], v[130:131], 1, s[26:27]
	v_add_u32_e32 v130, v142, v1
	v_cndmask_b32_e64 v130, 0, v130, s[8:9]
	global_load_ushort v178, v[132:133], off
	v_lshl_add_u64 v[132:133], v[130:131], 1, s[26:27]
	s_waitcnt lgkmcnt(1)
	v_add_u32_e32 v130, v136, v1
	s_waitcnt lgkmcnt(0)
	v_cmp_lt_u32_e64 s[4:5], v1, v137
	global_load_ushort v176, v[132:133], off
	v_add_u32_e32 v135, 0x18ba4, v134
	v_cndmask_b32_e64 v130, 0, v130, s[4:5]
	v_lshl_add_u64 v[132:133], v[130:131], 1, s[26:27]
	global_load_ushort v172, v[132:133], off
	v_add_u32_e32 v130, 0x19010, v134
	v_add_u32_e32 v132, 0x18b90, v134
	v_add_u32_e32 v136, 0x19038, v134
	v_add_u32_e32 v137, 0x18bb8, v134
	v_add_u32_e32 v138, 0x1904c, v134
	v_add_u32_e32 v139, 0x18bcc, v134
	v_add_u32_e32 v133, 0x19024, v134
	ds_read_b32 v130, v130
	ds_read_b32 v132, v132
	ds_read_b32 v140, v133
	ds_read_b32 v135, v135
	ds_read_b32 v136, v136
	ds_read_b32 v137, v137
	ds_read_b32 v138, v138
	ds_read_b32 v139, v139
	s_waitcnt lgkmcnt(7)
	v_add_u32_e32 v130, v130, v1
	s_waitcnt lgkmcnt(6)
	v_cmp_lt_u32_e64 s[20:21], v1, v132
	s_waitcnt lgkmcnt(4)
	v_cmp_lt_u32_e64 s[16:17], v1, v135
	s_waitcnt lgkmcnt(2)
	v_cmp_lt_u32_e64 s[10:11], v1, v137
	v_cndmask_b32_e64 v130, 0, v130, s[20:21]
	v_lshl_add_u64 v[132:133], v[130:131], 1, s[26:27]
	v_add_u32_e32 v130, v140, v1
	v_cndmask_b32_e64 v130, 0, v130, s[16:17]
	global_load_ushort v182, v[132:133], off
	v_lshl_add_u64 v[132:133], v[130:131], 1, s[26:27]
	v_add_u32_e32 v130, v136, v1
	v_cndmask_b32_e64 v130, 0, v130, s[10:11]
	global_load_ushort v179, v[132:133], off
	v_lshl_add_u64 v[132:133], v[130:131], 1, s[26:27]
	s_waitcnt lgkmcnt(1)
	v_add_u32_e32 v130, v138, v1
	s_waitcnt lgkmcnt(0)
	v_cmp_lt_u32_e64 s[6:7], v1, v139
	global_load_ushort v177, v[132:133], off
	v_add_u32_e32 v135, 0x18bf4, v134
	v_cndmask_b32_e64 v130, 0, v130, s[6:7]
	v_lshl_add_u64 v[132:133], v[130:131], 1, s[26:27]
	global_load_ushort v173, v[132:133], off
	v_or_b32_e32 v130, 0x19060, v134
	v_or_b32_e32 v132, 0x18be0, v134
	v_add_u32_e32 v133, 0x19074, v134
	v_add_u32_e32 v136, 0x19088, v134
	v_add_u32_e32 v134, 0x18c08, v134
	ds_read_b32 v130, v130
	ds_read_b32 v132, v132
	ds_read_b32 v137, v133
	ds_read_b32 v135, v135
	ds_read_b32 v136, v136
	ds_read_b32 v134, v134
	s_waitcnt lgkmcnt(5)
	v_add_u32_e32 v130, v130, v1
	s_waitcnt lgkmcnt(4)
	v_cmp_lt_u32_e64 s[14:15], v1, v132
	s_waitcnt lgkmcnt(2)
	v_cmp_lt_u32_e64 s[12:13], v1, v135
	s_movk_i32 s22, 0x4100
	v_cndmask_b32_e64 v130, 0, v130, s[14:15]
	v_lshl_add_u64 v[132:133], v[130:131], 1, s[26:27]
	v_add_u32_e32 v130, v137, v1
	v_cndmask_b32_e64 v130, 0, v130, s[12:13]
	global_load_ushort v180, v[132:133], off
	v_lshl_add_u64 v[132:133], v[130:131], 1, s[26:27]
	s_waitcnt lgkmcnt(1)
	v_add_u32_e32 v130, v136, v1
	s_waitcnt lgkmcnt(0)
	v_cmp_lt_u32_e64 s[0:1], v1, v134
	global_load_ushort v175, v[132:133], off
	v_lshrrev_b32_e32 v167, 4, v1
	v_cndmask_b32_e64 v130, 0, v130, s[0:1]
	v_lshl_add_u64 v[130:131], v[130:131], 1, s[26:27]
	global_load_ushort v174, v[130:131], off
	v_lshlrev_b32_e32 v130, 3, v1
	v_mad_u32_u24 v171, v164, s22, v130
	v_mul_u32_u24_e32 v130, 0x410, v166
	v_mad_u32_u24 v130, v164, s22, v130
	v_lshlrev_b32_e32 v131, 8, v167
	v_add_u32_e32 v168, v130, v131
	s_add_i32 s33, s30, 0x50
	s_add_i32 s31, s30, 0x58
	s_waitcnt vmcnt(27)
	v_cvt_pk_bf16_f32 v106, v106, v107
	v_cvt_pk_bf16_f32 v107, v108, v109
	v_cvt_pk_bf16_f32 v102, v102, v103
	v_cvt_pk_bf16_f32 v103, v104, v105
	ds_write2_b64 v171, v[106:107], v[102:103] offset0:130 offset1:194
	v_cvt_pk_bf16_f32 v102, v126, v127
	v_cvt_pk_bf16_f32 v103, v128, v129
	v_cvt_pk_bf16_f32 v104, v110, v111
	v_cvt_pk_bf16_f32 v105, v112, v113
	v_add_u32_e32 v106, 32, v171
	v_cvt_pk_bf16_f32 v86, v86, v87
	v_cvt_pk_bf16_f32 v87, v88, v89
	v_cvt_pk_bf16_f32 v78, v78, v79
	v_cvt_pk_bf16_f32 v79, v80, v81
	v_add_u32_e32 v80, 0x50, v171
	v_cvt_pk_bf16_f32 v122, v122, v123
	v_cvt_pk_bf16_f32 v123, v124, v125
	v_cvt_pk_bf16_f32 v118, v118, v119
	v_cvt_pk_bf16_f32 v119, v120, v121
	ds_write2st64_b64 v106, v[102:103], v[104:105] offset0:4 offset1:5
	v_cvt_pk_bf16_f32 v98, v98, v99
	v_cvt_pk_bf16_f32 v99, v100, v101
	v_cvt_pk_bf16_f32 v100, v114, v115
	v_cvt_pk_bf16_f32 v101, v116, v117
	v_add_u32_e32 v102, 48, v171
	v_cvt_pk_bf16_f32 v94, v94, v95
	v_cvt_pk_bf16_f32 v95, v96, v97
	v_cvt_pk_bf16_f32 v90, v90, v91
	v_cvt_pk_bf16_f32 v91, v92, v93
	v_add_u32_e32 v92, 64, v171
	ds_write2st64_b64 v80, v[86:87], v[78:79] offset0:10 offset1:11
	v_cvt_pk_bf16_f32 v78, v82, v83
	v_cvt_pk_bf16_f32 v79, v84, v85
	v_cvt_pk_bf16_f32 v74, v74, v75
	v_cvt_pk_bf16_f32 v75, v76, v77
	v_add_u32_e32 v76, 0x60, v171
	v_cvt_pk_bf16_f32 v70, v70, v71
	v_cvt_pk_bf16_f32 v71, v72, v73
	v_cvt_pk_bf16_f32 v66, v66, v67
	v_cvt_pk_bf16_f32 v67, v68, v69
	v_add_u32_e32 v68, 0x70, v171
	ds_write2st64_b64 v171, v[122:123], v[118:119] offset1:1
	ds_write2st64_b64 v102, v[98:99], v[100:101] offset0:6 offset1:7
	ds_write2st64_b64 v92, v[94:95], v[90:91] offset0:8 offset1:9
	ds_write2st64_b64 v76, v[78:79], v[74:75] offset0:12 offset1:13
	ds_write2st64_b64 v68, v[70:71], v[66:67] offset0:14 offset1:15
	v_add_u32_e32 v66, s33, v165
	v_min_i32_e32 v66, 0x18698, v66
	v_ashrrev_i32_e32 v67, 31, v66
	v_lshlrev_b64 v[66:67], 11, v[66:67]
	v_lshl_add_u64 v[66:67], v[162:163], 0, v[66:67]
	s_movk_i32 s34, 0x1000
	v_add_co_u32_e64 v68, s[22:23], s34, v66
	s_movk_i32 s35, 0x2000
	s_nop 0
	v_addc_co_u32_e64 v69, s[22:23], 0, v67, s[22:23]
	v_add_co_u32_e64 v98, s[22:23], s35, v66
	s_movk_i32 s36, 0x3000
	s_nop 0
	v_addc_co_u32_e64 v99, s[22:23], 0, v67, s[22:23]
	global_load_dwordx4 v[146:149], v[66:67], off nt
	global_load_dwordx4 v[138:141], v[66:67], off offset:1024 nt
	global_load_dwordx4 v[126:129], v[66:67], off offset:2048 nt
	global_load_dwordx4 v[118:121], v[66:67], off offset:3072 nt
	v_add_co_u32_e64 v66, s[22:23], s36, v66
	global_load_dwordx4 v[130:133], v[68:69], off offset:1024 nt
	global_load_dwordx4 v[102:105], v[68:69], off offset:2048 nt
	global_load_dwordx4 v[94:97], v[98:99], off nt
	global_load_dwordx4 v[90:93], v[98:99], off offset:1024 nt
	global_load_dwordx4 v[86:89], v[98:99], off offset:2048 nt
	global_load_dwordx4 v[78:81], v[98:99], off offset:3072 nt
	v_addc_co_u32_e64 v67, s[22:23], 0, v67, s[22:23]
	global_load_dwordx4 v[134:137], v[68:69], off offset:3072 nt
	global_load_dwordx4 v[82:85], v[66:67], off nt
	global_load_dwordx4 v[74:77], v[66:67], off offset:1024 nt
	global_load_dwordx4 v[70:73], v[66:67], off offset:2048 nt
	global_load_dwordx4 v[158:161], v[98:99], off offset:-4096 nt
	s_nop 0
	global_load_dwordx4 v[66:69], v[66:67], off offset:3072 nt
	s_waitcnt vmcnt(27)
	v_cvt_pk_bf16_f32 v50, v50, v51
	v_cvt_pk_bf16_f32 v51, v52, v53
	v_cvt_pk_bf16_f32 v38, v38, v39
	v_cvt_pk_bf16_f32 v39, v40, v41
	v_add_u32_e32 v40, 0x90, v171
	ds_write2st64_b64 v40, v[50:51], v[38:39] offset0:18 offset1:19
	v_cvt_pk_bf16_f32 v38, v62, v63
	v_cvt_pk_bf16_f32 v39, v64, v65
	v_cvt_pk_bf16_f32 v40, v42, v43
	v_cvt_pk_bf16_f32 v41, v44, v45
	v_add_u32_e32 v42, 0xa0, v171
	v_cvt_pk_bf16_f32 v22, v22, v23
	v_cvt_pk_bf16_f32 v23, v24, v25
	v_cvt_pk_bf16_f32 v14, v14, v15
	v_cvt_pk_bf16_f32 v15, v16, v17
	v_add_u32_e32 v16, 0xd0, v171
	v_cvt_pk_bf16_f32 v58, v58, v59
	v_cvt_pk_bf16_f32 v59, v60, v61
	v_cvt_pk_bf16_f32 v54, v54, v55
	v_cvt_pk_bf16_f32 v55, v56, v57
	v_add_u32_e32 v56, 0x80, v171
	ds_write2st64_b64 v42, v[38:39], v[40:41] offset0:20 offset1:21
	v_cvt_pk_bf16_f32 v34, v34, v35
	v_cvt_pk_bf16_f32 v35, v36, v37
	v_cvt_pk_bf16_f32 v36, v46, v47
	v_cvt_pk_bf16_f32 v37, v48, v49
	v_add_u32_e32 v38, 0xb0, v171
	v_cvt_pk_bf16_f32 v30, v30, v31
	v_cvt_pk_bf16_f32 v31, v32, v33
	v_cvt_pk_bf16_f32 v26, v26, v27
	v_cvt_pk_bf16_f32 v27, v28, v29
	v_add_u32_e32 v28, 0xc0, v171
	ds_write2st64_b64 v16, v[22:23], v[14:15] offset0:26 offset1:27
	v_cvt_pk_bf16_f32 v14, v18, v19
	v_cvt_pk_bf16_f32 v15, v20, v21
	v_cvt_pk_bf16_f32 v10, v10, v11
	v_cvt_pk_bf16_f32 v11, v12, v13
	v_add_u32_e32 v12, 0xe0, v171
	v_cvt_pk_bf16_f32 v6, v6, v7
	v_cvt_pk_bf16_f32 v7, v8, v9
	v_cvt_pk_bf16_f32 v2, v2, v3
	v_cvt_pk_bf16_f32 v3, v4, v5
	v_add_u32_e32 v4, 0xf0, v171
	ds_write2st64_b64 v56, v[58:59], v[54:55] offset0:16 offset1:17
	ds_write2st64_b64 v38, v[34:35], v[36:37] offset0:22 offset1:23
	ds_write2st64_b64 v28, v[30:31], v[26:27] offset0:24 offset1:25
	ds_write2st64_b64 v12, v[14:15], v[10:11] offset0:28 offset1:29
	ds_write2st64_b64 v4, v[6:7], v[2:3] offset0:30 offset1:31
	v_add_u32_e32 v2, s31, v165
	v_min_i32_e32 v2, 0x18698, v2
	v_ashrrev_i32_e32 v3, 31, v2
	v_lshlrev_b64 v[2:3], 11, v[2:3]
	v_lshl_add_u64 v[2:3], v[162:163], 0, v[2:3]
	v_add_co_u32_e64 v4, s[22:23], s34, v2
	global_load_dwordx4 v[150:153], v[2:3], off nt
	global_load_dwordx4 v[142:145], v[2:3], off offset:1024 nt
	global_load_dwordx4 v[122:125], v[2:3], off offset:2048 nt
	global_load_dwordx4 v[110:113], v[2:3], off offset:3072 nt
	v_addc_co_u32_e64 v5, s[22:23], 0, v3, s[22:23]
	v_add_co_u32_e64 v6, s[22:23], s35, v2
	s_nop 1
	v_addc_co_u32_e64 v7, s[22:23], 0, v3, s[22:23]
	v_add_co_u32_e64 v2, s[22:23], s36, v2
	global_load_dwordx4 v[114:117], v[4:5], off offset:1024 nt
	global_load_dwordx4 v[98:101], v[4:5], off offset:2048 nt
	global_load_dwordx4 v[50:53], v[6:7], off nt
	global_load_dwordx4 v[38:41], v[6:7], off offset:1024 nt
	global_load_dwordx4 v[34:37], v[6:7], off offset:2048 nt
	global_load_dwordx4 v[26:29], v[6:7], off offset:3072 nt
	v_addc_co_u32_e64 v3, s[22:23], 0, v3, s[22:23]
	global_load_dwordx4 v[106:109], v[4:5], off offset:3072 nt
	global_load_dwordx4 v[30:33], v[2:3], off nt
	global_load_dwordx4 v[14:17], v[2:3], off offset:1024 nt
	global_load_dwordx4 v[10:13], v[2:3], off offset:2048 nt
	global_load_dwordx4 v[154:157], v[6:7], off offset:-4096 nt
	s_nop 0
	global_load_dwordx4 v[6:9], v[2:3], off offset:3072 nt
	v_mov_b32_e32 v2, 0x14500
	v_lshl_add_u32 v54, v183, 4, v2
	ds_read_b128 v[2:5], v54
	ds_read_b128 v[18:21], v54 offset:1024
	ds_read_b128 v[22:25], v168
	ds_read_b128 v[42:45], v168 offset:16
	s_waitcnt lgkmcnt(1)
	v_mfma_f32_16x16x32_bf16 v[2:5], v[2:5], v[22:25], 0
	ds_read_b128 v[22:25], v54 offset:2048
	ds_read_b128 v[46:49], v54 offset:3072
	s_waitcnt lgkmcnt(2)
	v_mfma_f32_16x16x32_bf16 v[2:5], v[18:21], v[42:45], v[2:5]
	ds_read_b128 v[18:21], v168 offset:32
	ds_read_b128 v[42:45], v168 offset:48
	s_waitcnt lgkmcnt(1)
	v_mfma_f32_16x16x32_bf16 v[2:5], v[22:25], v[18:21], v[2:5]
	s_waitcnt lgkmcnt(0)
	v_mfma_f32_16x16x32_bf16 v[2:5], v[46:49], v[42:45], v[2:5]
	ds_read_b128 v[18:21], v54 offset:4096
	ds_read_b128 v[22:25], v54 offset:5120
	ds_read_b128 v[42:45], v168 offset:64
	ds_read_b128 v[46:49], v168 offset:80
	s_waitcnt lgkmcnt(1)
	v_mfma_f32_16x16x32_bf16 v[2:5], v[18:21], v[42:45], v[2:5]
	ds_read_b128 v[18:21], v54 offset:6144
	ds_read_b128 v[42:45], v54 offset:7168
	s_waitcnt lgkmcnt(2)
	v_mfma_f32_16x16x32_bf16 v[2:5], v[22:25], v[46:49], v[2:5]
	ds_read_b128 v[22:25], v168 offset:96
	ds_read_b128 v[46:49], v168 offset:112
	s_waitcnt lgkmcnt(1)
	v_mfma_f32_16x16x32_bf16 v[2:5], v[18:21], v[22:25], v[2:5]
	s_waitcnt lgkmcnt(0)
	v_mfma_f32_16x16x32_bf16 v[2:5], v[42:45], v[46:49], v[2:5]
	ds_read_b128 v[18:21], v54 offset:8192
	ds_read_b128 v[22:25], v54 offset:9216
	ds_read_b128 v[42:45], v168 offset:128
	ds_read_b128 v[46:49], v168 offset:144
	s_waitcnt lgkmcnt(1)
	v_mfma_f32_16x16x32_bf16 v[2:5], v[18:21], v[42:45], v[2:5]
	ds_read_b128 v[18:21], v54 offset:10240
	ds_read_b128 v[42:45], v54 offset:11264
	s_waitcnt lgkmcnt(2)
	v_mfma_f32_16x16x32_bf16 v[2:5], v[22:25], v[46:49], v[2:5]
	ds_read_b128 v[22:25], v168 offset:160
	ds_read_b128 v[46:49], v168 offset:176
	s_waitcnt lgkmcnt(1)
	v_mfma_f32_16x16x32_bf16 v[2:5], v[18:21], v[22:25], v[2:5]
	s_waitcnt lgkmcnt(0)
	v_mfma_f32_16x16x32_bf16 v[2:5], v[42:45], v[46:49], v[2:5]
	ds_read_b128 v[18:21], v54 offset:12288
	ds_read_b128 v[22:25], v54 offset:13312
	ds_read_b128 v[42:45], v168 offset:192
	ds_read_b128 v[46:49], v168 offset:208
	s_waitcnt lgkmcnt(1)
	v_mfma_f32_16x16x32_bf16 v[2:5], v[18:21], v[42:45], v[2:5]
	ds_read_b128 v[18:21], v54 offset:14336
	ds_read_b128 v[42:45], v54 offset:15360
	s_waitcnt lgkmcnt(2)
	v_mfma_f32_16x16x32_bf16 v[2:5], v[22:25], v[46:49], v[2:5]
	ds_read_b128 v[22:25], v168 offset:224
	ds_read_b128 v[46:49], v168 offset:240
	s_waitcnt lgkmcnt(1)
	v_mfma_f32_16x16x32_bf16 v[2:5], v[18:21], v[22:25], v[2:5]
	s_waitcnt lgkmcnt(0)
	v_mfma_f32_16x16x32_bf16 v[2:5], v[42:45], v[46:49], v[2:5]
	s_waitcnt vmcnt(42)
	v_cmp_ne_u16_e64 s[22:23], -1, v181
	s_and_b64 s[22:23], s[18:19], s[22:23]
	s_and_saveexec_b64 s[18:19], s[22:23]
	v_and_b32_e32 v18, 0xffff, v181
	v_mov_b32_e32 v19, 0x18500
	v_lshl_add_u32 v18, v18, 2, v19
	v_mov_b32_e32 v19, 1
	ds_add_u32 v18, v19
	s_or_b64 exec, exec, s[18:19]
	v_mov_b32_e32 v18, 0xffff
	s_mov_b32 s22, 0xffff
	s_waitcnt vmcnt(41)
	v_cndmask_b32_sdwa v19, v18, v178, vcc dst_sel:DWORD dst_unused:UNUSED_PAD src0_sel:DWORD src1_sel:WORD_0
	v_cmp_ne_u32_e32 vcc, s22, v19
	s_and_saveexec_b64 s[18:19], vcc
	v_mov_b32_e32 v20, 0x18500
	v_lshl_add_u32 v19, v19, 2, v20
	v_mov_b32_e32 v20, 1
	ds_add_u32 v19, v20
	s_or_b64 exec, exec, s[18:19]
	s_mov_b64 vcc, s[8:9]
	s_waitcnt vmcnt(40)
	v_cndmask_b32_sdwa v18, v18, v176, vcc dst_sel:DWORD dst_unused:UNUSED_PAD src0_sel:DWORD src1_sel:WORD_0
	v_cmp_ne_u32_e32 vcc, s22, v18
	s_and_saveexec_b64 s[8:9], vcc
	v_mov_b32_e32 v19, 0x18500
	v_lshl_add_u32 v18, v18, 2, v19
	v_mov_b32_e32 v19, 1
	ds_add_u32 v18, v19
	s_or_b64 exec, exec, s[8:9]
	s_mov_b64 vcc, s[4:5]
	v_mov_b32_e32 v18, 0xffff
	s_mov_b32 s8, 0xffff
	s_waitcnt vmcnt(39)
	v_cndmask_b32_sdwa v19, v18, v172, vcc dst_sel:DWORD dst_unused:UNUSED_PAD src0_sel:DWORD src1_sel:WORD_0
	v_cmp_ne_u32_e32 vcc, s8, v19
	s_and_saveexec_b64 s[4:5], vcc
	v_mov_b32_e32 v20, 0x18500
	v_lshl_add_u32 v19, v19, 2, v20
	v_mov_b32_e32 v20, 1
	ds_add_u32 v19, v20
	s_or_b64 exec, exec, s[4:5]
	s_mov_b64 vcc, s[20:21]
	s_waitcnt vmcnt(38)
	v_cndmask_b32_sdwa v18, v18, v182, vcc dst_sel:DWORD dst_unused:UNUSED_PAD src0_sel:DWORD src1_sel:WORD_0
	v_cmp_ne_u32_e32 vcc, s8, v18
	s_and_saveexec_b64 s[4:5], vcc
	v_mov_b32_e32 v19, 0x18500
	v_lshl_add_u32 v18, v18, 2, v19
	v_mov_b32_e32 v19, 1
	ds_add_u32 v18, v19
	s_or_b64 exec, exec, s[4:5]
	s_mov_b64 vcc, s[16:17]
	v_mov_b32_e32 v18, 0xffff
	s_waitcnt vmcnt(37)
	v_cndmask_b32_sdwa v19, v18, v179, vcc dst_sel:DWORD dst_unused:UNUSED_PAD src0_sel:DWORD src1_sel:WORD_0
	v_cmp_ne_u32_e32 vcc, s8, v19
	s_and_saveexec_b64 s[4:5], vcc
	v_mov_b32_e32 v20, 0x18500
	v_lshl_add_u32 v19, v19, 2, v20
	v_mov_b32_e32 v20, 1
	ds_add_u32 v19, v20
	s_or_b64 exec, exec, s[4:5]
	s_mov_b64 vcc, s[10:11]
	s_waitcnt vmcnt(36)
	v_cndmask_b32_sdwa v18, v18, v177, vcc dst_sel:DWORD dst_unused:UNUSED_PAD src0_sel:DWORD src1_sel:WORD_0
	v_cmp_ne_u32_e32 vcc, s8, v18
	s_and_saveexec_b64 s[4:5], vcc
	v_mov_b32_e32 v19, 0x18500
	v_lshl_add_u32 v18, v18, 2, v19
	v_mov_b32_e32 v19, 1
	ds_add_u32 v18, v19
	s_or_b64 exec, exec, s[4:5]
	s_mov_b64 vcc, s[6:7]
	v_mov_b32_e32 v18, 0xffff
	s_mov_b32 s6, 0xffff
	s_waitcnt vmcnt(35)
	v_cndmask_b32_sdwa v19, v18, v173, vcc dst_sel:DWORD dst_unused:UNUSED_PAD src0_sel:DWORD src1_sel:WORD_0
	v_cmp_ne_u32_e32 vcc, s6, v19
	s_and_saveexec_b64 s[4:5], vcc
	v_mov_b32_e32 v20, 0x18500
	v_lshl_add_u32 v19, v19, 2, v20
	v_mov_b32_e32 v20, 1
	ds_add_u32 v19, v20
	s_or_b64 exec, exec, s[4:5]
	s_mov_b64 vcc, s[14:15]
	s_waitcnt vmcnt(34)
	v_cndmask_b32_sdwa v18, v18, v180, vcc dst_sel:DWORD dst_unused:UNUSED_PAD src0_sel:DWORD src1_sel:WORD_0
	v_cmp_ne_u32_e32 vcc, s6, v18
	s_and_saveexec_b64 s[4:5], vcc
	v_mov_b32_e32 v19, 0x18500
	v_lshl_add_u32 v18, v18, 2, v19
	v_mov_b32_e32 v19, 1
	ds_add_u32 v18, v19
	s_or_b64 exec, exec, s[4:5]
	s_mov_b64 vcc, s[12:13]
	v_mov_b32_e32 v18, 0xffff
	s_waitcnt vmcnt(33)
	v_cndmask_b32_sdwa v19, v18, v175, vcc dst_sel:DWORD dst_unused:UNUSED_PAD src0_sel:DWORD src1_sel:WORD_0
	v_cmp_ne_u32_e32 vcc, s6, v19
	s_and_saveexec_b64 s[4:5], vcc
	v_mov_b32_e32 v20, 0x18500
	v_lshl_add_u32 v19, v19, 2, v20
	v_mov_b32_e32 v20, 1
	ds_add_u32 v19, v20
	s_or_b64 exec, exec, s[4:5]
	s_mov_b64 vcc, s[0:1]
	s_waitcnt vmcnt(32)
	v_cndmask_b32_sdwa v18, v18, v174, vcc dst_sel:DWORD dst_unused:UNUSED_PAD src0_sel:DWORD src1_sel:WORD_0
	v_cmp_ne_u32_e32 vcc, s6, v18
	s_and_saveexec_b64 s[0:1], vcc
	v_mov_b32_e32 v19, 0x18500
	v_lshl_add_u32 v18, v18, 2, v19
	v_mov_b32_e32 v19, 1
	ds_add_u32 v18, v19
	s_or_b64 exec, exec, s[0:1]
	v_mov_b32_e32 v183, v1
	ds_read2_b32 v[18:19], v169 offset0:55 offset1:60
	ds_read2_b32 v[20:21], v170 offset0:55 offset1:60
	ds_read2_b32 v[22:23], v170 offset0:65 offset1:70
	ds_read2_b32 v[24:25], v169 offset0:65 offset1:70
	v_mov_b32_e32 v43, 0
	s_waitcnt lgkmcnt(3)
	v_add_u32_e32 v18, v18, v1
	s_waitcnt lgkmcnt(2)
	v_cmp_lt_u32_e64 s[20:21], v1, v20
	s_waitcnt lgkmcnt(1)
	v_cmp_lt_u32_e64 s[16:17], v1, v22
	s_waitcnt lgkmcnt(0)
	v_add_u32_e32 v20, v24, v1
	v_add_u32_e32 v22, v25, v1
	ds_read2_b32 v[24:25], v169 offset0:75 offset1:80
	ds_read2_b32 v[46:47], v170 offset0:75 offset1:80
	v_cndmask_b32_e64 v42, 0, v18, s[20:21]
	v_add_u32_e32 v18, v19, v1
	v_cmp_lt_u32_e32 vcc, v1, v21
	v_lshl_add_u64 v[44:45], v[42:43], 1, s[26:27]
	v_cmp_lt_u32_e64 s[18:19], v1, v23
	v_cndmask_b32_e32 v42, 0, v18, vcc
	v_lshl_add_u64 v[18:19], v[42:43], 1, s[26:27]
	v_cndmask_b32_e64 v42, 0, v20, s[16:17]
	v_lshl_add_u64 v[20:21], v[42:43], 1, s[26:27]
	v_cndmask_b32_e64 v42, 0, v22, s[18:19]
	s_waitcnt lgkmcnt(1)
	v_add_u32_e32 v24, v24, v1
	s_waitcnt lgkmcnt(0)
	v_cmp_lt_u32_e64 s[12:13], v1, v46
	v_lshl_add_u64 v[22:23], v[42:43], 1, s[26:27]
	v_cmp_lt_u32_e64 s[14:15], v1, v47
	v_cndmask_b32_e64 v42, 0, v24, s[12:13]
	v_lshl_add_u64 v[48:49], v[42:43], 1, s[26:27]
	v_add_u32_e32 v42, v25, v1
	ds_read2_b32 v[24:25], v169 offset0:85 offset1:90
	ds_read2_b32 v[54:55], v170 offset0:85 offset1:90
	v_cndmask_b32_e64 v42, 0, v42, s[14:15]
	v_lshl_add_u64 v[46:47], v[42:43], 1, s[26:27]
	s_waitcnt lgkmcnt(1)
	v_add_u32_e32 v24, v24, v1
	s_waitcnt lgkmcnt(0)
	v_cmp_lt_u32_e64 s[10:11], v1, v54
	v_cmp_lt_u32_e64 s[4:5], v1, v55
	ds_read2_b32 v[54:55], v169 offset0:95 offset1:100
	ds_read2_b32 v[58:59], v170 offset0:95 offset1:100
	v_cndmask_b32_e64 v42, 0, v24, s[10:11]
	v_add_u32_e32 v24, v25, v1
	v_lshl_add_u64 v[56:57], v[42:43], 1, s[26:27]
	v_cndmask_b32_e64 v42, 0, v24, s[4:5]
	v_lshl_add_u64 v[24:25], v[42:43], 1, s[26:27]
	global_load_ushort v182, v[44:45], off
	global_load_ushort v181, v[18:19], off
	global_load_ushort v180, v[20:21], off
	global_load_ushort v179, v[22:23], off
	global_load_ushort v178, v[48:49], off
	global_load_ushort v177, v[46:47], off
	global_load_ushort v176, v[56:57], off
	global_load_ushort v174, v[24:25], off
	ds_read_b32 v22, v169 offset:420
	ds_read_b32 v23, v170 offset:420
	s_waitcnt lgkmcnt(3)
	v_add_u32_e32 v18, v54, v1
	s_waitcnt lgkmcnt(2)
	v_cmp_lt_u32_e64 s[6:7], v1, v58
	v_add_u32_e32 v20, v55, v1
	v_cmp_lt_u32_e64 s[8:9], v1, v59
	v_cndmask_b32_e64 v42, 0, v18, s[6:7]
	v_lshl_add_u64 v[18:19], v[42:43], 1, s[26:27]
	v_cndmask_b32_e64 v42, 0, v20, s[8:9]
	s_waitcnt lgkmcnt(1)
	v_add_u32_e32 v22, v22, v1
	s_waitcnt lgkmcnt(0)
	v_cmp_lt_u32_e64 s[0:1], v1, v23
	v_lshl_add_u64 v[20:21], v[42:43], 1, s[26:27]
	s_nop 0
	v_cndmask_b32_e64 v42, 0, v22, s[0:1]
	v_lshl_add_u64 v[22:23], v[42:43], 1, s[26:27]
	global_load_ushort v175, v[18:19], off
	global_load_ushort v173, v[20:21], off
	global_load_ushort v172, v[22:23], off
	s_waitcnt vmcnt(42)
	v_cvt_pk_bf16_f32 v18, v146, v147
	v_cvt_pk_bf16_f32 v19, v148, v149
	s_waitcnt vmcnt(41)
	v_cvt_pk_bf16_f32 v20, v138, v139
	v_cvt_pk_bf16_f32 v21, v140, v141
	ds_write2st64_b64 v171, v[18:19], v[20:21] offset1:1
	s_waitcnt vmcnt(40)
	v_cvt_pk_bf16_f32 v18, v126, v127
	v_cvt_pk_bf16_f32 v19, v128, v129
	s_waitcnt vmcnt(39)
	v_cvt_pk_bf16_f32 v20, v118, v119
	v_cvt_pk_bf16_f32 v21, v120, v121
	ds_write2_b64 v171, v[18:19], v[20:21] offset0:130 offset1:194
	s_waitcnt vmcnt(28)
	v_cvt_pk_bf16_f32 v18, v158, v159
	v_cvt_pk_bf16_f32 v19, v160, v161
	v_cvt_pk_bf16_f32 v20, v130, v131
	v_cvt_pk_bf16_f32 v21, v132, v133
	v_add_u32_e32 v22, 32, v171
	ds_write2st64_b64 v22, v[18:19], v[20:21] offset0:4 offset1:5
	v_cvt_pk_bf16_f32 v18, v102, v103
	v_cvt_pk_bf16_f32 v19, v104, v105
	v_cvt_pk_bf16_f32 v20, v134, v135
	v_cvt_pk_bf16_f32 v21, v136, v137
	v_add_u32_e32 v22, 48, v171
	ds_write2st64_b64 v22, v[18:19], v[20:21] offset0:6 offset1:7
	v_cvt_pk_bf16_f32 v18, v94, v95
	v_cvt_pk_bf16_f32 v19, v96, v97
	v_cvt_pk_bf16_f32 v20, v90, v91
	v_cvt_pk_bf16_f32 v21, v92, v93
	v_add_u32_e32 v22, 64, v171
	ds_write2st64_b64 v22, v[18:19], v[20:21] offset0:8 offset1:9
	v_cvt_pk_bf16_f32 v18, v86, v87
	v_cvt_pk_bf16_f32 v19, v88, v89
	v_cvt_pk_bf16_f32 v20, v78, v79
	v_cvt_pk_bf16_f32 v21, v80, v81
	v_add_u32_e32 v22, 0x50, v171
	ds_write2st64_b64 v22, v[18:19], v[20:21] offset0:10 offset1:11
	v_cvt_pk_bf16_f32 v18, v82, v83
	v_cvt_pk_bf16_f32 v19, v84, v85
	v_cvt_pk_bf16_f32 v20, v74, v75
	v_cvt_pk_bf16_f32 v21, v76, v77
	v_add_u32_e32 v22, 0x60, v171
	ds_write2st64_b64 v22, v[18:19], v[20:21] offset0:12 offset1:13
	v_cvt_pk_bf16_f32 v18, v70, v71
	v_cvt_pk_bf16_f32 v19, v72, v73
	s_waitcnt vmcnt(27)
	v_cvt_pk_bf16_f32 v20, v66, v67
	v_cvt_pk_bf16_f32 v21, v68, v69
	v_add_u32_e32 v22, 0x70, v171
	ds_write2st64_b64 v22, v[18:19], v[20:21] offset0:14 offset1:15
	v_mov_b32_e32 v18, 0x50
	v_lshl_add_u32 v158, v164, 4, v18
	v_add_u32_e32 v18, s33, v158
	v_min_i32_e32 v18, 0x18698, v18
	v_ashrrev_i32_e32 v19, 31, v18
	v_lshlrev_b64 v[18:19], 11, v[18:19]
	v_lshl_add_u64 v[18:19], v[162:163], 0, v[18:19]
	v_add_co_u32_e64 v20, s[22:23], s34, v18
	global_load_dwordx4 v[134:137], v[18:19], off nt
	global_load_dwordx4 v[130:133], v[18:19], off offset:1024 nt
	global_load_dwordx4 v[102:105], v[18:19], off offset:2048 nt
	global_load_dwordx4 v[90:93], v[18:19], off offset:3072 nt
	v_addc_co_u32_e64 v21, s[22:23], 0, v19, s[22:23]
	v_add_co_u32_e64 v66, s[22:23], s35, v18
	s_nop 1
	v_addc_co_u32_e64 v67, s[22:23], 0, v19, s[22:23]
	v_add_co_u32_e64 v18, s[22:23], s36, v18
	global_load_dwordx4 v[118:121], v[20:21], off offset:1024 nt
	global_load_dwordx4 v[78:81], v[20:21], off offset:2048 nt
	global_load_dwordx4 v[74:77], v[66:67], off nt
	global_load_dwordx4 v[62:65], v[66:67], off offset:1024 nt
	global_load_dwordx4 v[58:61], v[66:67], off offset:2048 nt
	global_load_dwordx4 v[46:49], v[66:67], off offset:3072 nt
	v_addc_co_u32_e64 v19, s[22:23], 0, v19, s[22:23]
	global_load_dwordx4 v[126:129], v[20:21], off offset:3072 nt
	global_load_dwordx4 v[54:57], v[18:19], off nt
	global_load_dwordx4 v[42:45], v[18:19], off offset:1024 nt
	global_load_dwordx4 v[22:25], v[18:19], off offset:2048 nt
	global_load_dwordx4 v[146:149], v[66:67], off offset:-4096 nt
	s_nop 0
	global_load_dwordx4 v[18:21], v[18:19], off offset:3072 nt
	s_waitcnt vmcnt(42)
	v_cvt_pk_bf16_f32 v66, v150, v151
	v_cvt_pk_bf16_f32 v67, v152, v153
	s_waitcnt vmcnt(41)
	v_cvt_pk_bf16_f32 v68, v142, v143
	v_cvt_pk_bf16_f32 v69, v144, v145
	v_add_u32_e32 v70, 0x80, v171
	ds_write2st64_b64 v70, v[66:67], v[68:69] offset0:16 offset1:17
	s_waitcnt vmcnt(40)
	v_cvt_pk_bf16_f32 v66, v122, v123
	v_cvt_pk_bf16_f32 v67, v124, v125
	s_waitcnt vmcnt(39)
	v_cvt_pk_bf16_f32 v68, v110, v111
	v_cvt_pk_bf16_f32 v69, v112, v113
	v_add_u32_e32 v70, 0x90, v171
	ds_write2st64_b64 v70, v[66:67], v[68:69] offset0:18 offset1:19
	s_waitcnt vmcnt(28)
	v_cvt_pk_bf16_f32 v66, v154, v155
	v_cvt_pk_bf16_f32 v67, v156, v157
	v_cvt_pk_bf16_f32 v68, v114, v115
	v_cvt_pk_bf16_f32 v69, v116, v117
	v_add_u32_e32 v70, 0xa0, v171
	v_cvt_pk_bf16_f32 v34, v34, v35
	v_cvt_pk_bf16_f32 v35, v36, v37
	v_cvt_pk_bf16_f32 v26, v26, v27
	v_cvt_pk_bf16_f32 v27, v28, v29
	v_add_u32_e32 v28, 0xd0, v171
	ds_write2st64_b64 v70, v[66:67], v[68:69] offset0:20 offset1:21
	v_cvt_pk_bf16_f32 v66, v98, v99
	v_cvt_pk_bf16_f32 v67, v100, v101
	v_cvt_pk_bf16_f32 v68, v106, v107
	v_cvt_pk_bf16_f32 v69, v108, v109
	v_add_u32_e32 v70, 0xb0, v171
	v_cvt_pk_bf16_f32 v50, v50, v51
	v_cvt_pk_bf16_f32 v51, v52, v53
	v_cvt_pk_bf16_f32 v38, v38, v39
	v_cvt_pk_bf16_f32 v39, v40, v41
	v_add_u32_e32 v40, 0xc0, v171
	ds_write2st64_b64 v28, v[34:35], v[26:27] offset0:26 offset1:27
	v_cvt_pk_bf16_f32 v26, v30, v31
	v_cvt_pk_bf16_f32 v27, v32, v33
	v_cvt_pk_bf16_f32 v14, v14, v15
	v_cvt_pk_bf16_f32 v15, v16, v17
	v_add_u32_e32 v16, 0xe0, v171
	v_cvt_pk_bf16_f32 v10, v10, v11
	v_cvt_pk_bf16_f32 v11, v12, v13
	s_waitcnt vmcnt(27)
	v_cvt_pk_bf16_f32 v6, v6, v7
	v_cvt_pk_bf16_f32 v7, v8, v9
	v_add_u32_e32 v8, 0xf0, v171
	ds_write2st64_b64 v70, v[66:67], v[68:69] offset0:22 offset1:23
	ds_write2st64_b64 v40, v[50:51], v[38:39] offset0:24 offset1:25
	ds_write2st64_b64 v16, v[26:27], v[14:15] offset0:28 offset1:29
	ds_write2st64_b64 v8, v[10:11], v[6:7] offset0:30 offset1:31
	v_add_u32_e32 v6, s31, v158
	v_min_i32_e32 v6, 0x18698, v6
	v_ashrrev_i32_e32 v7, 31, v6
	v_lshlrev_b64 v[6:7], 11, v[6:7]
	v_lshl_add_u64 v[6:7], v[162:163], 0, v[6:7]
	v_add_co_u32_e64 v8, s[22:23], s34, v6
	global_load_dwordx4 v[138:141], v[6:7], off nt
	global_load_dwordx4 v[114:117], v[6:7], off offset:1024 nt
	global_load_dwordx4 v[106:109], v[6:7], off offset:2048 nt
	global_load_dwordx4 v[94:97], v[6:7], off offset:3072 nt
	v_addc_co_u32_e64 v9, s[22:23], 0, v7, s[22:23]
	v_add_co_u32_e64 v10, s[22:23], s35, v6
	s_nop 1
	v_addc_co_u32_e64 v11, s[22:23], 0, v7, s[22:23]
	v_add_co_u32_e64 v6, s[22:23], s36, v6
	global_load_dwordx4 v[98:101], v[8:9], off offset:1024 nt
	global_load_dwordx4 v[82:85], v[8:9], off offset:2048 nt
	global_load_dwordx4 v[70:73], v[10:11], off nt
	global_load_dwordx4 v[66:69], v[10:11], off offset:1024 nt
	global_load_dwordx4 v[50:53], v[10:11], off offset:2048 nt
	global_load_dwordx4 v[34:37], v[10:11], off offset:3072 nt
	v_addc_co_u32_e64 v7, s[22:23], 0, v7, s[22:23]
	global_load_dwordx4 v[86:89], v[8:9], off offset:3072 nt
	global_load_dwordx4 v[38:41], v[6:7], off nt
	global_load_dwordx4 v[26:29], v[6:7], off offset:1024 nt
	global_load_dwordx4 v[14:17], v[6:7], off offset:2048 nt
	global_load_dwordx4 v[142:145], v[10:11], off offset:-4096 nt
	s_nop 0
	global_load_dwordx4 v[10:13], v[6:7], off offset:3072 nt
	v_mov_b32_e32 v6, 0x14500
	v_lshl_add_u32 v154, v183, 4, v6
	ds_read_b128 v[6:9], v154
	ds_read_b128 v[30:33], v154 offset:1024
	ds_read_b128 v[110:113], v168
	ds_read_b128 v[122:125], v168 offset:16
	s_waitcnt lgkmcnt(1)
	v_mfma_f32_16x16x32_bf16 v[6:9], v[6:9], v[110:113], 0
	ds_read_b128 v[110:113], v154 offset:2048
	ds_read_b128 v[150:153], v154 offset:3072
	s_waitcnt lgkmcnt(2)
	v_mfma_f32_16x16x32_bf16 v[6:9], v[30:33], v[122:125], v[6:9]
	ds_read_b128 v[30:33], v168 offset:32
	ds_read_b128 v[122:125], v168 offset:48
	s_waitcnt lgkmcnt(1)
	v_mfma_f32_16x16x32_bf16 v[6:9], v[110:113], v[30:33], v[6:9]
	s_waitcnt lgkmcnt(0)
	v_mfma_f32_16x16x32_bf16 v[6:9], v[150:153], v[122:125], v[6:9]
	ds_read_b128 v[30:33], v154 offset:4096
	ds_read_b128 v[110:113], v154 offset:5120
	ds_read_b128 v[122:125], v168 offset:64
	ds_read_b128 v[150:153], v168 offset:80
	s_waitcnt lgkmcnt(1)
	v_mfma_f32_16x16x32_bf16 v[6:9], v[30:33], v[122:125], v[6:9]
	ds_read_b128 v[30:33], v154 offset:6144
	ds_read_b128 v[122:125], v154 offset:7168
	s_waitcnt lgkmcnt(2)
	v_mfma_f32_16x16x32_bf16 v[6:9], v[110:113], v[150:153], v[6:9]
	ds_read_b128 v[110:113], v168 offset:96
	ds_read_b128 v[150:153], v168 offset:112
	s_waitcnt lgkmcnt(1)
	v_mfma_f32_16x16x32_bf16 v[6:9], v[30:33], v[110:113], v[6:9]
	s_waitcnt lgkmcnt(0)
	v_mfma_f32_16x16x32_bf16 v[6:9], v[122:125], v[150:153], v[6:9]
	ds_read_b128 v[30:33], v154 offset:8192
	ds_read_b128 v[110:113], v154 offset:9216
	ds_read_b128 v[122:125], v168 offset:128
	ds_read_b128 v[150:153], v168 offset:144
	s_waitcnt lgkmcnt(1)
	v_mfma_f32_16x16x32_bf16 v[6:9], v[30:33], v[122:125], v[6:9]
	ds_read_b128 v[30:33], v154 offset:10240
	ds_read_b128 v[122:125], v154 offset:11264
	s_waitcnt lgkmcnt(2)
	v_mfma_f32_16x16x32_bf16 v[6:9], v[110:113], v[150:153], v[6:9]
	ds_read_b128 v[110:113], v168 offset:160
	ds_read_b128 v[150:153], v168 offset:176
	s_waitcnt lgkmcnt(1)
	v_mfma_f32_16x16x32_bf16 v[6:9], v[30:33], v[110:113], v[6:9]
	s_waitcnt lgkmcnt(0)
	v_mfma_f32_16x16x32_bf16 v[6:9], v[122:125], v[150:153], v[6:9]
	ds_read_b128 v[30:33], v154 offset:12288
	ds_read_b128 v[110:113], v154 offset:13312
	ds_read_b128 v[122:125], v168 offset:192
	ds_read_b128 v[150:153], v168 offset:208
	s_waitcnt lgkmcnt(1)
	v_mfma_f32_16x16x32_bf16 v[6:9], v[30:33], v[122:125], v[6:9]
	ds_read_b128 v[30:33], v154 offset:14336
	ds_read_b128 v[122:125], v154 offset:15360
	s_waitcnt lgkmcnt(2)
	v_mfma_f32_16x16x32_bf16 v[6:9], v[110:113], v[150:153], v[6:9]
	ds_read_b128 v[110:113], v168 offset:224
	ds_read_b128 v[150:153], v168 offset:240
	s_waitcnt lgkmcnt(1)
	v_mfma_f32_16x16x32_bf16 v[6:9], v[30:33], v[110:113], v[6:9]
	s_waitcnt lgkmcnt(0)
	v_mfma_f32_16x16x32_bf16 v[6:9], v[122:125], v[150:153], v[6:9]
	s_waitcnt vmcnt(42)
	v_cmp_ne_u16_e64 s[22:23], -1, v182
	s_and_b64 s[22:23], s[20:21], s[22:23]
	s_and_saveexec_b64 s[20:21], s[22:23]
	v_and_b32_e32 v30, 0xffff, v182
	v_mov_b32_e32 v31, 0x18500
	v_lshl_add_u32 v30, v30, 2, v31
	v_mov_b32_e32 v31, 1
	ds_add_u32 v30, v31
	s_or_b64 exec, exec, s[20:21]
	v_mov_b32_e32 v30, 0xffff
	s_mov_b32 s22, 0xffff
	s_waitcnt vmcnt(41)
	v_cndmask_b32_sdwa v31, v30, v181, vcc dst_sel:DWORD dst_unused:UNUSED_PAD src0_sel:DWORD src1_sel:WORD_0
	v_cmp_ne_u32_e32 vcc, s22, v31
	s_and_saveexec_b64 s[20:21], vcc
	v_mov_b32_e32 v32, 0x18500
	v_lshl_add_u32 v31, v31, 2, v32
	v_mov_b32_e32 v32, 1
	ds_add_u32 v31, v32
	s_or_b64 exec, exec, s[20:21]
	s_mov_b64 vcc, s[16:17]
	s_waitcnt vmcnt(40)
	v_cndmask_b32_sdwa v30, v30, v180, vcc dst_sel:DWORD dst_unused:UNUSED_PAD src0_sel:DWORD src1_sel:WORD_0
	v_cmp_ne_u32_e32 vcc, s22, v30
	s_and_saveexec_b64 s[16:17], vcc
	v_mov_b32_e32 v31, 0x18500
	v_lshl_add_u32 v30, v30, 2, v31
	v_mov_b32_e32 v31, 1
	ds_add_u32 v30, v31
	s_or_b64 exec, exec, s[16:17]
	s_mov_b64 vcc, s[18:19]
	v_mov_b32_e32 v30, 0xffff
	s_mov_b32 s18, 0xffff
	s_waitcnt vmcnt(39)
	v_cndmask_b32_sdwa v31, v30, v179, vcc dst_sel:DWORD dst_unused:UNUSED_PAD src0_sel:DWORD src1_sel:WORD_0
	v_cmp_ne_u32_e32 vcc, s18, v31
	s_and_saveexec_b64 s[16:17], vcc
	v_mov_b32_e32 v32, 0x18500
	v_lshl_add_u32 v31, v31, 2, v32
	v_mov_b32_e32 v32, 1
	ds_add_u32 v31, v32
	s_or_b64 exec, exec, s[16:17]
	s_mov_b64 vcc, s[12:13]
	s_waitcnt vmcnt(38)
	v_cndmask_b32_sdwa v30, v30, v178, vcc dst_sel:DWORD dst_unused:UNUSED_PAD src0_sel:DWORD src1_sel:WORD_0
	v_cmp_ne_u32_e32 vcc, s18, v30
	s_and_saveexec_b64 s[12:13], vcc
	v_mov_b32_e32 v31, 0x18500
	v_lshl_add_u32 v30, v30, 2, v31
	v_mov_b32_e32 v31, 1
	ds_add_u32 v30, v31
	s_or_b64 exec, exec, s[12:13]
	s_mov_b64 vcc, s[14:15]
	v_mov_b32_e32 v30, 0xffff
	s_mov_b32 s14, 0xffff
	s_waitcnt vmcnt(37)
	v_cndmask_b32_sdwa v31, v30, v177, vcc dst_sel:DWORD dst_unused:UNUSED_PAD src0_sel:DWORD src1_sel:WORD_0
	v_cmp_ne_u32_e32 vcc, s14, v31
	s_and_saveexec_b64 s[12:13], vcc
	v_mov_b32_e32 v32, 0x18500
	v_lshl_add_u32 v31, v31, 2, v32
	v_mov_b32_e32 v32, 1
	ds_add_u32 v31, v32
	s_or_b64 exec, exec, s[12:13]
	s_mov_b64 vcc, s[10:11]
	s_waitcnt vmcnt(36)
	v_cndmask_b32_sdwa v30, v30, v176, vcc dst_sel:DWORD dst_unused:UNUSED_PAD src0_sel:DWORD src1_sel:WORD_0
	v_cmp_ne_u32_e32 vcc, s14, v30
	s_and_saveexec_b64 s[10:11], vcc
	v_mov_b32_e32 v31, 0x18500
	v_lshl_add_u32 v30, v30, 2, v31
	v_mov_b32_e32 v31, 1
	ds_add_u32 v30, v31
	s_or_b64 exec, exec, s[10:11]
	s_mov_b64 vcc, s[4:5]
	v_mov_b32_e32 v30, 0xffff
	s_mov_b32 s10, 0xffff
	s_waitcnt vmcnt(35)
	v_cndmask_b32_sdwa v31, v30, v174, vcc dst_sel:DWORD dst_unused:UNUSED_PAD src0_sel:DWORD src1_sel:WORD_0
	v_cmp_ne_u32_e32 vcc, s10, v31
	s_and_saveexec_b64 s[4:5], vcc
	v_mov_b32_e32 v32, 0x18500
	v_lshl_add_u32 v31, v31, 2, v32
	v_mov_b32_e32 v32, 1
	ds_add_u32 v31, v32
	s_or_b64 exec, exec, s[4:5]
	s_mov_b64 vcc, s[6:7]
	s_waitcnt vmcnt(34)
	v_cndmask_b32_sdwa v30, v30, v175, vcc dst_sel:DWORD dst_unused:UNUSED_PAD src0_sel:DWORD src1_sel:WORD_0
	v_cmp_ne_u32_e32 vcc, s10, v30
	s_and_saveexec_b64 s[4:5], vcc
	v_mov_b32_e32 v31, 0x18500
	v_lshl_add_u32 v30, v30, 2, v31
	v_mov_b32_e32 v31, 1
	ds_add_u32 v30, v31
	s_or_b64 exec, exec, s[4:5]
	s_mov_b64 vcc, s[8:9]
	v_mov_b32_e32 v30, 0xffff
	s_mov_b32 s6, 0xffff
	s_waitcnt vmcnt(33)
	v_cndmask_b32_sdwa v31, v30, v173, vcc dst_sel:DWORD dst_unused:UNUSED_PAD src0_sel:DWORD src1_sel:WORD_0
	v_cmp_ne_u32_e32 vcc, s6, v31
	s_and_saveexec_b64 s[4:5], vcc
	v_mov_b32_e32 v32, 0x18500
	v_lshl_add_u32 v31, v31, 2, v32
	v_mov_b32_e32 v32, 1
	ds_add_u32 v31, v32
	s_or_b64 exec, exec, s[4:5]
	s_mov_b64 vcc, s[0:1]
	s_waitcnt vmcnt(32)
	v_cndmask_b32_sdwa v30, v30, v172, vcc dst_sel:DWORD dst_unused:UNUSED_PAD src0_sel:DWORD src1_sel:WORD_0
	v_cmp_ne_u32_e32 vcc, s6, v30
	s_and_saveexec_b64 s[0:1], vcc
	v_mov_b32_e32 v31, 0x18500
	v_lshl_add_u32 v30, v30, 2, v31
	v_mov_b32_e32 v31, 1
	ds_add_u32 v30, v31
	s_or_b64 exec, exec, s[0:1]
	v_mov_b32_e32 v173, v1
	ds_read2_b32 v[30:31], v169 offset0:110 offset1:115
	ds_read2_b32 v[32:33], v170 offset0:110 offset1:115
	ds_read2_b32 v[110:111], v170 offset0:120 offset1:125
	ds_read2_b32 v[112:113], v169 offset0:120 offset1:125
	v_mov_b32_e32 v123, 0
	s_waitcnt lgkmcnt(3)
	v_add_u32_e32 v30, v30, v1
	s_waitcnt lgkmcnt(2)
	v_cmp_lt_u32_e64 s[20:21], v1, v32
	s_waitcnt lgkmcnt(1)
	v_cmp_lt_u32_e64 s[16:17], v1, v110
	s_waitcnt lgkmcnt(0)
	v_add_u32_e32 v32, v112, v1
	v_add_u32_e32 v110, v113, v1
	ds_read2_b32 v[112:113], v169 offset0:130 offset1:135
	ds_read2_b32 v[150:151], v170 offset0:130 offset1:135
	v_cndmask_b32_e64 v122, 0, v30, s[20:21]
	v_add_u32_e32 v30, v31, v1
	v_cmp_lt_u32_e32 vcc, v1, v33
	v_lshl_add_u64 v[124:125], v[122:123], 1, s[26:27]
	v_cmp_lt_u32_e64 s[18:19], v1, v111
	v_cndmask_b32_e32 v122, 0, v30, vcc
	v_lshl_add_u64 v[30:31], v[122:123], 1, s[26:27]
	v_cndmask_b32_e64 v122, 0, v32, s[16:17]
	v_lshl_add_u64 v[32:33], v[122:123], 1, s[26:27]
	v_cndmask_b32_e64 v122, 0, v110, s[18:19]
	s_waitcnt lgkmcnt(1)
	v_add_u32_e32 v112, v112, v1
	s_waitcnt lgkmcnt(0)
	v_cmp_lt_u32_e64 s[12:13], v1, v150
	v_lshl_add_u64 v[110:111], v[122:123], 1, s[26:27]
	v_cmp_lt_u32_e64 s[14:15], v1, v151
	v_cndmask_b32_e64 v122, 0, v112, s[12:13]
	v_lshl_add_u64 v[152:153], v[122:123], 1, s[26:27]
	v_add_u32_e32 v122, v113, v1
	ds_read2_b32 v[112:113], v169 offset0:140 offset1:145
	ds_read2_b32 v[154:155], v170 offset0:140 offset1:145
	v_cndmask_b32_e64 v122, 0, v122, s[14:15]
	v_lshl_add_u64 v[150:151], v[122:123], 1, s[26:27]
	ds_read2_b32 v[176:177], v169 offset0:150 offset1:155
	ds_read2_b32 v[178:179], v170 offset0:150 offset1:155
	s_waitcnt lgkmcnt(3)
	v_add_u32_e32 v112, v112, v1
	s_waitcnt lgkmcnt(2)
	v_cmp_lt_u32_e64 s[10:11], v1, v154
	v_cmp_lt_u32_e64 s[4:5], v1, v155
	s_waitcnt lgkmcnt(0)
	v_cmp_lt_u32_e64 s[6:7], v1, v178
	v_cndmask_b32_e64 v122, 0, v112, s[10:11]
	v_add_u32_e32 v112, v113, v1
	v_lshl_add_u64 v[174:175], v[122:123], 1, s[26:27]
	v_cndmask_b32_e64 v122, 0, v112, s[4:5]
	v_lshl_add_u64 v[112:113], v[122:123], 1, s[26:27]
	global_load_ushort v172, v[124:125], off
	global_load_ushort v161, v[30:31], off
	global_load_ushort v160, v[32:33], off
	global_load_ushort v159, v[110:111], off
	global_load_ushort v157, v[152:153], off
	global_load_ushort v156, v[150:151], off
	global_load_ushort v155, v[174:175], off
	s_nop 0
	global_load_ushort v153, v[112:113], off
	ds_read_b32 v110, v169 offset:640
	ds_read_b32 v111, v170 offset:640
	v_add_u32_e32 v30, v176, v1
	v_cndmask_b32_e64 v122, 0, v30, s[6:7]
	v_add_u32_e32 v32, v177, v1
	v_cmp_lt_u32_e64 s[8:9], v1, v179
	v_lshl_add_u64 v[30:31], v[122:123], 1, s[26:27]
	s_waitcnt lgkmcnt(1)
	v_add_u32_e32 v110, v110, v1
	v_cndmask_b32_e64 v122, 0, v32, s[8:9]
	s_waitcnt lgkmcnt(0)
	v_cmp_lt_u32_e64 s[0:1], v1, v111
	v_lshl_add_u64 v[32:33], v[122:123], 1, s[26:27]
	s_nop 0
	v_cndmask_b32_e64 v122, 0, v110, s[0:1]
	v_lshl_add_u64 v[110:111], v[122:123], 1, s[26:27]
	global_load_ushort v154, v[30:31], off
	global_load_ushort v152, v[32:33], off
	global_load_ushort v151, v[110:111], off
	s_waitcnt vmcnt(42)
	v_cvt_pk_bf16_f32 v30, v134, v135
	v_cvt_pk_bf16_f32 v31, v136, v137
	s_waitcnt vmcnt(41)
	v_cvt_pk_bf16_f32 v32, v130, v131
	v_cvt_pk_bf16_f32 v33, v132, v133
	ds_write2st64_b64 v171, v[30:31], v[32:33] offset1:1
	s_waitcnt vmcnt(40)
	v_cvt_pk_bf16_f32 v30, v102, v103
	v_cvt_pk_bf16_f32 v31, v104, v105
	s_waitcnt vmcnt(39)
	v_cvt_pk_bf16_f32 v32, v90, v91
	v_cvt_pk_bf16_f32 v33, v92, v93
	ds_write2_b64 v171, v[30:31], v[32:33] offset0:130 offset1:194
	s_waitcnt vmcnt(28)
	v_cvt_pk_bf16_f32 v30, v146, v147
	v_cvt_pk_bf16_f32 v31, v148, v149
	v_cvt_pk_bf16_f32 v32, v118, v119
	v_cvt_pk_bf16_f32 v33, v120, v121
	v_add_u32_e32 v90, 32, v171
	ds_write2st64_b64 v90, v[30:31], v[32:33] offset0:4 offset1:5
	v_cvt_pk_bf16_f32 v30, v78, v79
	v_cvt_pk_bf16_f32 v31, v80, v81
	v_cvt_pk_bf16_f32 v32, v126, v127
	v_cvt_pk_bf16_f32 v33, v128, v129
	v_add_u32_e32 v78, 48, v171
	ds_write2st64_b64 v78, v[30:31], v[32:33] offset0:6 offset1:7
	v_cvt_pk_bf16_f32 v30, v74, v75
	v_cvt_pk_bf16_f32 v31, v76, v77
	v_cvt_pk_bf16_f32 v32, v62, v63
	v_cvt_pk_bf16_f32 v33, v64, v65
	v_add_u32_e32 v62, 64, v171
	ds_write2st64_b64 v62, v[30:31], v[32:33] offset0:8 offset1:9
	v_cvt_pk_bf16_f32 v30, v58, v59
	v_cvt_pk_bf16_f32 v31, v60, v61
	v_cvt_pk_bf16_f32 v32, v46, v47
	v_cvt_pk_bf16_f32 v33, v48, v49
	v_add_u32_e32 v46, 0x50, v171
	ds_write2st64_b64 v46, v[30:31], v[32:33] offset0:10 offset1:11
	v_cvt_pk_bf16_f32 v30, v54, v55
	v_cvt_pk_bf16_f32 v31, v56, v57
	v_cvt_pk_bf16_f32 v32, v42, v43
	v_cvt_pk_bf16_f32 v33, v44, v45
	v_add_u32_e32 v42, 0x60, v171
	v_cvt_pk_bf16_f32 v22, v22, v23
	v_cvt_pk_bf16_f32 v23, v24, v25
	s_waitcnt vmcnt(27)
	v_cvt_pk_bf16_f32 v18, v18, v19
	v_cvt_pk_bf16_f32 v19, v20, v21
	v_add_u32_e32 v20, 0x70, v171
	ds_write2st64_b64 v42, v[30:31], v[32:33] offset0:12 offset1:13
	ds_write2st64_b64 v20, v[22:23], v[18:19] offset0:14 offset1:15
	v_mov_b32_e32 v18, 0xa0
	v_lshl_add_u32 v150, v164, 4, v18
	v_add_u32_e32 v18, s33, v150
	v_min_i32_e32 v18, 0x18698, v18
	v_ashrrev_i32_e32 v19, 31, v18
	v_lshlrev_b64 v[18:19], 11, v[18:19]
	v_lshl_add_u64 v[18:19], v[162:163], 0, v[18:19]
	v_add_co_u32_e64 v20, s[22:23], s34, v18
	global_load_dwordx4 v[134:137], v[18:19], off nt
	global_load_dwordx4 v[126:129], v[18:19], off offset:1024 nt
	global_load_dwordx4 v[110:113], v[18:19], off offset:2048 nt
	global_load_dwordx4 v[102:105], v[18:19], off offset:3072 nt
	v_addc_co_u32_e64 v21, s[22:23], 0, v19, s[22:23]
	v_add_co_u32_e64 v22, s[22:23], s35, v18
	s_nop 1
	v_addc_co_u32_e64 v23, s[22:23], 0, v19, s[22:23]
	v_add_co_u32_e64 v18, s[22:23], s36, v18
	global_load_dwordx4 v[118:121], v[20:21], off offset:1024 nt
	global_load_dwordx4 v[90:93], v[20:21], off offset:2048 nt
	global_load_dwordx4 v[78:81], v[22:23], off nt
	global_load_dwordx4 v[74:77], v[22:23], off offset:1024 nt
	global_load_dwordx4 v[62:65], v[22:23], off offset:2048 nt
	global_load_dwordx4 v[54:57], v[22:23], off offset:3072 nt
	v_addc_co_u32_e64 v19, s[22:23], 0, v19, s[22:23]
	global_load_dwordx4 v[122:125], v[20:21], off offset:3072 nt
	global_load_dwordx4 v[58:61], v[18:19], off nt
	global_load_dwordx4 v[46:49], v[18:19], off offset:1024 nt
	global_load_dwordx4 v[30:33], v[18:19], off offset:2048 nt
	global_load_dwordx4 v[146:149], v[22:23], off offset:-4096 nt
	s_nop 0
	global_load_dwordx4 v[22:25], v[18:19], off offset:3072 nt
	s_waitcnt vmcnt(42)
	v_cvt_pk_bf16_f32 v18, v138, v139
	v_cvt_pk_bf16_f32 v19, v140, v141
	s_waitcnt vmcnt(41)
	v_cvt_pk_bf16_f32 v20, v114, v115
	v_cvt_pk_bf16_f32 v21, v116, v117
	v_add_u32_e32 v42, 0x80, v171
	ds_write2st64_b64 v42, v[18:19], v[20:21] offset0:16 offset1:17
	s_waitcnt vmcnt(40)
	v_cvt_pk_bf16_f32 v18, v106, v107
	v_cvt_pk_bf16_f32 v19, v108, v109
	s_waitcnt vmcnt(39)
	v_cvt_pk_bf16_f32 v20, v94, v95
	v_cvt_pk_bf16_f32 v21, v96, v97
	v_add_u32_e32 v42, 0x90, v171
	ds_write2st64_b64 v42, v[18:19], v[20:21] offset0:18 offset1:19
	s_waitcnt vmcnt(28)
	v_cvt_pk_bf16_f32 v18, v142, v143
	v_cvt_pk_bf16_f32 v19, v144, v145
	v_cvt_pk_bf16_f32 v20, v98, v99
	v_cvt_pk_bf16_f32 v21, v100, v101
	v_add_u32_e32 v42, 0xa0, v171
	ds_write2st64_b64 v42, v[18:19], v[20:21] offset0:20 offset1:21
	v_cvt_pk_bf16_f32 v18, v82, v83
	v_cvt_pk_bf16_f32 v19, v84, v85
	v_cvt_pk_bf16_f32 v20, v86, v87
	v_cvt_pk_bf16_f32 v21, v88, v89
	v_add_u32_e32 v42, 0xb0, v171
	ds_write2st64_b64 v42, v[18:19], v[20:21] offset0:22 offset1:23
	v_cvt_pk_bf16_f32 v18, v70, v71
	v_cvt_pk_bf16_f32 v19, v72, v73
	v_cvt_pk_bf16_f32 v20, v66, v67
	v_cvt_pk_bf16_f32 v21, v68, v69
	v_add_u32_e32 v42, 0xc0, v171
	ds_write2st64_b64 v42, v[18:19], v[20:21] offset0:24 offset1:25
	v_cvt_pk_bf16_f32 v18, v50, v51
	v_cvt_pk_bf16_f32 v19, v52, v53
	v_cvt_pk_bf16_f32 v20, v34, v35
	v_cvt_pk_bf16_f32 v21, v36, v37
	v_add_u32_e32 v34, 0xd0, v171
	ds_write2st64_b64 v34, v[18:19], v[20:21] offset0:26 offset1:27
	v_cvt_pk_bf16_f32 v18, v38, v39
	v_cvt_pk_bf16_f32 v19, v40, v41
	v_cvt_pk_bf16_f32 v20, v26, v27
	v_cvt_pk_bf16_f32 v21, v28, v29
	v_add_u32_e32 v26, 0xe0, v171
	v_cvt_pk_bf16_f32 v14, v14, v15
	v_cvt_pk_bf16_f32 v15, v16, v17
	s_waitcnt vmcnt(27)
	v_cvt_pk_bf16_f32 v10, v10, v11
	v_cvt_pk_bf16_f32 v11, v12, v13
	v_add_u32_e32 v12, 0xf0, v171
	ds_write2st64_b64 v26, v[18:19], v[20:21] offset0:28 offset1:29
	ds_write2st64_b64 v12, v[14:15], v[10:11] offset0:30 offset1:31
	v_add_u32_e32 v10, s31, v150
	v_min_i32_e32 v10, 0x18698, v10
	v_ashrrev_i32_e32 v11, 31, v10
	v_lshlrev_b64 v[10:11], 11, v[10:11]
	v_lshl_add_u64 v[10:11], v[162:163], 0, v[10:11]
	v_add_co_u32_e64 v12, s[22:23], s34, v10
	global_load_dwordx4 v[138:141], v[10:11], off nt
	global_load_dwordx4 v[130:133], v[10:11], off offset:1024 nt
	global_load_dwordx4 v[114:117], v[10:11], off offset:2048 nt
	global_load_dwordx4 v[94:97], v[10:11], off offset:3072 nt
	v_addc_co_u32_e64 v13, s[22:23], 0, v11, s[22:23]
	v_add_co_u32_e64 v14, s[22:23], s35, v10
	s_nop 1
	v_addc_co_u32_e64 v15, s[22:23], 0, v11, s[22:23]
	v_add_co_u32_e64 v10, s[22:23], s36, v10
	global_load_dwordx4 v[98:101], v[12:13], off offset:1024 nt
	global_load_dwordx4 v[82:85], v[12:13], off offset:2048 nt
	global_load_dwordx4 v[70:73], v[14:15], off nt
	global_load_dwordx4 v[66:69], v[14:15], off offset:1024 nt
	global_load_dwordx4 v[50:53], v[14:15], off offset:2048 nt
	global_load_dwordx4 v[38:41], v[14:15], off offset:3072 nt
	v_addc_co_u32_e64 v11, s[22:23], 0, v11, s[22:23]
	global_load_dwordx4 v[86:89], v[12:13], off offset:3072 nt
	global_load_dwordx4 v[42:45], v[10:11], off nt
	global_load_dwordx4 v[34:37], v[10:11], off offset:1024 nt
	global_load_dwordx4 v[18:21], v[10:11], off offset:2048 nt
	global_load_dwordx4 v[142:145], v[14:15], off offset:-4096 nt
	s_nop 0
	global_load_dwordx4 v[14:17], v[10:11], off offset:3072 nt
	v_mov_b32_e32 v10, 0x14500
	v_lshl_add_u32 v173, v173, 4, v10
	ds_read_b128 v[10:13], v173
	ds_read_b128 v[26:29], v173 offset:1024
	ds_read_b128 v[106:109], v168
	ds_read_b128 v[174:177], v168 offset:16
	s_waitcnt lgkmcnt(1)
	v_mfma_f32_16x16x32_bf16 v[10:13], v[10:13], v[106:109], 0
	ds_read_b128 v[106:109], v173 offset:2048
	ds_read_b128 v[178:181], v173 offset:3072
	s_waitcnt lgkmcnt(2)
	v_mfma_f32_16x16x32_bf16 v[10:13], v[26:29], v[174:177], v[10:13]
	ds_read_b128 v[26:29], v168 offset:32
	ds_read_b128 v[174:177], v168 offset:48
	s_waitcnt lgkmcnt(1)
	v_mfma_f32_16x16x32_bf16 v[10:13], v[106:109], v[26:29], v[10:13]
	s_waitcnt lgkmcnt(0)
	v_mfma_f32_16x16x32_bf16 v[10:13], v[178:181], v[174:177], v[10:13]
	ds_read_b128 v[26:29], v173 offset:4096
	ds_read_b128 v[106:109], v173 offset:5120
	ds_read_b128 v[174:177], v168 offset:64
	ds_read_b128 v[178:181], v168 offset:80
	s_waitcnt lgkmcnt(1)
	v_mfma_f32_16x16x32_bf16 v[10:13], v[26:29], v[174:177], v[10:13]
	ds_read_b128 v[26:29], v173 offset:6144
	ds_read_b128 v[174:177], v173 offset:7168
	s_waitcnt lgkmcnt(2)
	v_mfma_f32_16x16x32_bf16 v[10:13], v[106:109], v[178:181], v[10:13]
	ds_read_b128 v[106:109], v168 offset:96
	ds_read_b128 v[178:181], v168 offset:112
	s_waitcnt lgkmcnt(1)
	v_mfma_f32_16x16x32_bf16 v[10:13], v[26:29], v[106:109], v[10:13]
	s_waitcnt lgkmcnt(0)
	v_mfma_f32_16x16x32_bf16 v[10:13], v[174:177], v[178:181], v[10:13]
	ds_read_b128 v[26:29], v173 offset:8192
	ds_read_b128 v[106:109], v173 offset:9216
	ds_read_b128 v[174:177], v168 offset:128
	ds_read_b128 v[178:181], v168 offset:144
	s_waitcnt lgkmcnt(1)
	v_mfma_f32_16x16x32_bf16 v[10:13], v[26:29], v[174:177], v[10:13]
	ds_read_b128 v[26:29], v173 offset:10240
	ds_read_b128 v[174:177], v173 offset:11264
	s_waitcnt lgkmcnt(2)
	v_mfma_f32_16x16x32_bf16 v[10:13], v[106:109], v[178:181], v[10:13]
	ds_read_b128 v[106:109], v168 offset:160
	ds_read_b128 v[178:181], v168 offset:176
	s_waitcnt lgkmcnt(1)
	v_mfma_f32_16x16x32_bf16 v[10:13], v[26:29], v[106:109], v[10:13]
	s_waitcnt lgkmcnt(0)
	v_mfma_f32_16x16x32_bf16 v[10:13], v[174:177], v[178:181], v[10:13]
	ds_read_b128 v[26:29], v173 offset:12288
	ds_read_b128 v[106:109], v173 offset:13312
	ds_read_b128 v[174:177], v168 offset:192
	ds_read_b128 v[178:181], v168 offset:208
	s_waitcnt lgkmcnt(1)
	v_mfma_f32_16x16x32_bf16 v[10:13], v[26:29], v[174:177], v[10:13]
	ds_read_b128 v[26:29], v173 offset:14336
	ds_read_b128 v[174:177], v173 offset:15360
	s_waitcnt lgkmcnt(2)
	v_mfma_f32_16x16x32_bf16 v[10:13], v[106:109], v[178:181], v[10:13]
	ds_read_b128 v[106:109], v168 offset:224
	ds_read_b128 v[178:181], v168 offset:240
	s_waitcnt lgkmcnt(1)
	v_mfma_f32_16x16x32_bf16 v[10:13], v[26:29], v[106:109], v[10:13]
	s_waitcnt lgkmcnt(0)
	v_mfma_f32_16x16x32_bf16 v[10:13], v[174:177], v[178:181], v[10:13]
	s_waitcnt vmcnt(42)
	v_cmp_ne_u16_e64 s[22:23], -1, v172
	s_and_b64 s[22:23], s[20:21], s[22:23]
	s_and_saveexec_b64 s[20:21], s[22:23]
	v_and_b32_e32 v26, 0xffff, v172
	v_mov_b32_e32 v27, 0x18500
	v_lshl_add_u32 v26, v26, 2, v27
	v_mov_b32_e32 v27, 1
	ds_add_u32 v26, v27
	s_or_b64 exec, exec, s[20:21]
	v_mov_b32_e32 v26, 0xffff
	s_mov_b32 s22, 0xffff
	s_waitcnt vmcnt(41)
	v_cndmask_b32_sdwa v27, v26, v161, vcc dst_sel:DWORD dst_unused:UNUSED_PAD src0_sel:DWORD src1_sel:WORD_0
	v_cmp_ne_u32_e32 vcc, s22, v27
	s_and_saveexec_b64 s[20:21], vcc
	v_mov_b32_e32 v28, 0x18500
	v_lshl_add_u32 v27, v27, 2, v28
	v_mov_b32_e32 v28, 1
	ds_add_u32 v27, v28
	s_or_b64 exec, exec, s[20:21]
	s_mov_b64 vcc, s[16:17]
	s_waitcnt vmcnt(40)
	v_cndmask_b32_sdwa v26, v26, v160, vcc dst_sel:DWORD dst_unused:UNUSED_PAD src0_sel:DWORD src1_sel:WORD_0
	v_cmp_ne_u32_e32 vcc, s22, v26
	s_and_saveexec_b64 s[16:17], vcc
	v_mov_b32_e32 v27, 0x18500
	v_lshl_add_u32 v26, v26, 2, v27
	v_mov_b32_e32 v27, 1
	ds_add_u32 v26, v27
	s_or_b64 exec, exec, s[16:17]
	s_mov_b64 vcc, s[18:19]
	v_mov_b32_e32 v26, 0xffff
	s_mov_b32 s18, 0xffff
	s_waitcnt vmcnt(39)
	v_cndmask_b32_sdwa v27, v26, v159, vcc dst_sel:DWORD dst_unused:UNUSED_PAD src0_sel:DWORD src1_sel:WORD_0
	v_cmp_ne_u32_e32 vcc, s18, v27
	s_and_saveexec_b64 s[16:17], vcc
	v_mov_b32_e32 v28, 0x18500
	v_lshl_add_u32 v27, v27, 2, v28
	v_mov_b32_e32 v28, 1
	ds_add_u32 v27, v28
	s_or_b64 exec, exec, s[16:17]
	s_mov_b64 vcc, s[12:13]
	s_waitcnt vmcnt(38)
	v_cndmask_b32_sdwa v26, v26, v157, vcc dst_sel:DWORD dst_unused:UNUSED_PAD src0_sel:DWORD src1_sel:WORD_0
	v_cmp_ne_u32_e32 vcc, s18, v26
	s_and_saveexec_b64 s[12:13], vcc
	v_mov_b32_e32 v27, 0x18500
	v_lshl_add_u32 v26, v26, 2, v27
	v_mov_b32_e32 v27, 1
	ds_add_u32 v26, v27
	s_or_b64 exec, exec, s[12:13]
	s_mov_b64 vcc, s[14:15]
	v_mov_b32_e32 v26, 0xffff
	s_mov_b32 s14, 0xffff
	s_waitcnt vmcnt(37)
	v_cndmask_b32_sdwa v27, v26, v156, vcc dst_sel:DWORD dst_unused:UNUSED_PAD src0_sel:DWORD src1_sel:WORD_0
	v_cmp_ne_u32_e32 vcc, s14, v27
	s_and_saveexec_b64 s[12:13], vcc
	v_mov_b32_e32 v28, 0x18500
	v_lshl_add_u32 v27, v27, 2, v28
	v_mov_b32_e32 v28, 1
	ds_add_u32 v27, v28
	s_or_b64 exec, exec, s[12:13]
	s_mov_b64 vcc, s[10:11]
	s_waitcnt vmcnt(36)
	v_cndmask_b32_sdwa v26, v26, v155, vcc dst_sel:DWORD dst_unused:UNUSED_PAD src0_sel:DWORD src1_sel:WORD_0
	v_cmp_ne_u32_e32 vcc, s14, v26
	s_and_saveexec_b64 s[10:11], vcc
	v_mov_b32_e32 v27, 0x18500
	v_lshl_add_u32 v26, v26, 2, v27
	v_mov_b32_e32 v27, 1
	ds_add_u32 v26, v27
	s_or_b64 exec, exec, s[10:11]
	s_mov_b64 vcc, s[4:5]
	v_mov_b32_e32 v26, 0xffff
	s_mov_b32 s10, 0xffff
	s_waitcnt vmcnt(35)
	v_cndmask_b32_sdwa v27, v26, v153, vcc dst_sel:DWORD dst_unused:UNUSED_PAD src0_sel:DWORD src1_sel:WORD_0
	v_cmp_ne_u32_e32 vcc, s10, v27
	s_and_saveexec_b64 s[4:5], vcc
	v_mov_b32_e32 v28, 0x18500
	v_lshl_add_u32 v27, v27, 2, v28
	v_mov_b32_e32 v28, 1
	ds_add_u32 v27, v28
	s_or_b64 exec, exec, s[4:5]
	s_mov_b64 vcc, s[6:7]
	s_waitcnt vmcnt(34)
	v_cndmask_b32_sdwa v26, v26, v154, vcc dst_sel:DWORD dst_unused:UNUSED_PAD src0_sel:DWORD src1_sel:WORD_0
	v_cmp_ne_u32_e32 vcc, s10, v26
	s_and_saveexec_b64 s[4:5], vcc
	v_mov_b32_e32 v27, 0x18500
	v_lshl_add_u32 v26, v26, 2, v27
	v_mov_b32_e32 v27, 1
	ds_add_u32 v26, v27
	s_or_b64 exec, exec, s[4:5]
	s_mov_b64 vcc, s[8:9]
	v_mov_b32_e32 v26, 0xffff
	s_mov_b32 s6, 0xffff
	s_waitcnt vmcnt(33)
	v_cndmask_b32_sdwa v27, v26, v152, vcc dst_sel:DWORD dst_unused:UNUSED_PAD src0_sel:DWORD src1_sel:WORD_0
	v_cmp_ne_u32_e32 vcc, s6, v27
	s_and_saveexec_b64 s[4:5], vcc
	v_mov_b32_e32 v28, 0x18500
	v_lshl_add_u32 v27, v27, 2, v28
	v_mov_b32_e32 v28, 1
	ds_add_u32 v27, v28
	s_or_b64 exec, exec, s[4:5]
	s_mov_b64 vcc, s[0:1]
	s_waitcnt vmcnt(32)
	v_cndmask_b32_sdwa v26, v26, v151, vcc dst_sel:DWORD dst_unused:UNUSED_PAD src0_sel:DWORD src1_sel:WORD_0
	v_cmp_ne_u32_e32 vcc, s6, v26
	s_and_saveexec_b64 s[0:1], vcc
	v_mov_b32_e32 v27, 0x18500
	v_lshl_add_u32 v26, v26, 2, v27
	v_mov_b32_e32 v27, 1
	ds_add_u32 v26, v27
	s_or_b64 exec, exec, s[0:1]
	v_mov_b32_e32 v173, v1
	ds_read2_b32 v[26:27], v169 offset0:165 offset1:170
	ds_read2_b32 v[28:29], v170 offset0:165 offset1:170
	ds_read2_b32 v[106:107], v170 offset0:175 offset1:180
	ds_read2_b32 v[108:109], v169 offset0:175 offset1:180
	v_mov_b32_e32 v175, 0
	s_waitcnt lgkmcnt(3)
	v_add_u32_e32 v26, v26, v1
	s_waitcnt lgkmcnt(2)
	v_cmp_lt_u32_e64 s[20:21], v1, v28
	s_waitcnt lgkmcnt(1)
	v_cmp_lt_u32_e64 s[16:17], v1, v106
	s_waitcnt lgkmcnt(0)
	v_add_u32_e32 v28, v108, v1
	v_add_u32_e32 v106, v109, v1
	ds_read2_b32 v[108:109], v169 offset0:185 offset1:190
	ds_read2_b32 v[154:155], v170 offset0:185 offset1:190
	v_cndmask_b32_e64 v174, 0, v26, s[20:21]
	v_add_u32_e32 v26, v27, v1
	v_cmp_lt_u32_e32 vcc, v1, v29
	v_lshl_add_u64 v[152:153], v[174:175], 1, s[26:27]
	v_cmp_lt_u32_e64 s[18:19], v1, v107
	v_cndmask_b32_e32 v174, 0, v26, vcc
	v_lshl_add_u64 v[26:27], v[174:175], 1, s[26:27]
	v_cndmask_b32_e64 v174, 0, v28, s[16:17]
	v_lshl_add_u64 v[28:29], v[174:175], 1, s[26:27]
	v_cndmask_b32_e64 v174, 0, v106, s[18:19]
	s_waitcnt lgkmcnt(1)
	v_add_u32_e32 v108, v108, v1
	s_waitcnt lgkmcnt(0)
	v_cmp_lt_u32_e64 s[12:13], v1, v154
	v_lshl_add_u64 v[106:107], v[174:175], 1, s[26:27]
	v_add_u32_e32 v151, v109, v1
	v_cndmask_b32_e64 v174, 0, v108, s[12:13]
	ds_read2_b32 v[108:109], v169 offset0:195 offset1:200
	ds_read2_b32 v[160:161], v170 offset0:195 offset1:200
	v_cmp_lt_u32_e64 s[14:15], v1, v155
	v_lshl_add_u64 v[156:157], v[174:175], 1, s[26:27]
	ds_read2_b32 v[178:179], v169 offset0:205 offset1:210
	ds_read2_b32 v[180:181], v170 offset0:205 offset1:210
	v_cndmask_b32_e64 v174, 0, v151, s[14:15]
	s_waitcnt lgkmcnt(3)
	v_add_u32_e32 v108, v108, v1
	s_waitcnt lgkmcnt(2)
	v_cmp_lt_u32_e64 s[10:11], v1, v160
	v_lshl_add_u64 v[154:155], v[174:175], 1, s[26:27]
	v_cmp_lt_u32_e64 s[4:5], v1, v161
	v_cndmask_b32_e64 v174, 0, v108, s[10:11]
	v_add_u32_e32 v108, v109, v1
	v_lshl_add_u64 v[176:177], v[174:175], 1, s[26:27]
	v_cndmask_b32_e64 v174, 0, v108, s[4:5]
	v_lshl_add_u64 v[108:109], v[174:175], 1, s[26:27]
	global_load_ushort v172, v[152:153], off
	global_load_ushort v161, v[26:27], off
	global_load_ushort v160, v[28:29], off
	global_load_ushort v159, v[106:107], off
	s_nop 0
	global_load_ushort v157, v[156:157], off
	s_nop 0
	global_load_ushort v156, v[154:155], off
	s_nop 0
	global_load_ushort v155, v[176:177], off
	global_load_ushort v153, v[108:109], off
	ds_read_b32 v106, v169 offset:860
	ds_read_b32 v107, v170 offset:860
	s_waitcnt lgkmcnt(3)
	v_add_u32_e32 v26, v178, v1
	s_waitcnt lgkmcnt(2)
	v_cmp_lt_u32_e64 s[6:7], v1, v180
	v_add_u32_e32 v28, v179, v1
	v_cmp_lt_u32_e64 s[8:9], v1, v181
	v_cndmask_b32_e64 v174, 0, v26, s[6:7]
	v_lshl_add_u64 v[26:27], v[174:175], 1, s[26:27]
	v_cndmask_b32_e64 v174, 0, v28, s[8:9]
	s_waitcnt lgkmcnt(1)
	v_add_u32_e32 v106, v106, v1
	s_waitcnt lgkmcnt(0)
	v_cmp_lt_u32_e64 s[0:1], v1, v107
	v_lshl_add_u64 v[28:29], v[174:175], 1, s[26:27]
	s_nop 0
	v_cndmask_b32_e64 v174, 0, v106, s[0:1]
	v_lshl_add_u64 v[106:107], v[174:175], 1, s[26:27]
	global_load_ushort v154, v[26:27], off
	global_load_ushort v152, v[28:29], off
	global_load_ushort v151, v[106:107], off
	s_waitcnt vmcnt(42)
	v_cvt_pk_bf16_f32 v26, v134, v135
	v_cvt_pk_bf16_f32 v27, v136, v137
	s_waitcnt vmcnt(41)
	v_cvt_pk_bf16_f32 v28, v126, v127
	v_cvt_pk_bf16_f32 v29, v128, v129
	ds_write2st64_b64 v171, v[26:27], v[28:29] offset1:1
	s_waitcnt vmcnt(40)
	v_cvt_pk_bf16_f32 v26, v110, v111
	v_cvt_pk_bf16_f32 v27, v112, v113
	s_waitcnt vmcnt(39)
	v_cvt_pk_bf16_f32 v28, v102, v103
	v_cvt_pk_bf16_f32 v29, v104, v105
	ds_write2_b64 v171, v[26:27], v[28:29] offset0:130 offset1:194
	s_waitcnt vmcnt(28)
	v_cvt_pk_bf16_f32 v26, v146, v147
	v_cvt_pk_bf16_f32 v27, v148, v149
	v_cvt_pk_bf16_f32 v28, v118, v119
	v_cvt_pk_bf16_f32 v29, v120, v121
	v_add_u32_e32 v102, 32, v171
	ds_write2st64_b64 v102, v[26:27], v[28:29] offset0:4 offset1:5
	v_cvt_pk_bf16_f32 v26, v90, v91
	v_cvt_pk_bf16_f32 v27, v92, v93
	v_cvt_pk_bf16_f32 v28, v122, v123
	v_cvt_pk_bf16_f32 v29, v124, v125
	v_add_u32_e32 v90, 48, v171
	ds_write2st64_b64 v90, v[26:27], v[28:29] offset0:6 offset1:7
	v_cvt_pk_bf16_f32 v26, v78, v79
	v_cvt_pk_bf16_f32 v27, v80, v81
	v_cvt_pk_bf16_f32 v28, v74, v75
	v_cvt_pk_bf16_f32 v29, v76, v77
	v_add_u32_e32 v74, 64, v171
	ds_write2st64_b64 v74, v[26:27], v[28:29] offset0:8 offset1:9
	v_cvt_pk_bf16_f32 v26, v62, v63
	v_cvt_pk_bf16_f32 v27, v64, v65
	v_cvt_pk_bf16_f32 v28, v54, v55
	v_cvt_pk_bf16_f32 v29, v56, v57
	v_add_u32_e32 v54, 0x50, v171
	ds_write2st64_b64 v54, v[26:27], v[28:29] offset0:10 offset1:11
	v_cvt_pk_bf16_f32 v26, v58, v59
	v_cvt_pk_bf16_f32 v27, v60, v61
	v_cvt_pk_bf16_f32 v28, v46, v47
	v_cvt_pk_bf16_f32 v29, v48, v49
	v_add_u32_e32 v46, 0x60, v171
	ds_write2st64_b64 v46, v[26:27], v[28:29] offset0:12 offset1:13
	v_cvt_pk_bf16_f32 v26, v30, v31
	v_cvt_pk_bf16_f32 v27, v32, v33
	s_waitcnt vmcnt(27)
	v_cvt_pk_bf16_f32 v22, v22, v23
	v_cvt_pk_bf16_f32 v23, v24, v25
	v_add_u32_e32 v24, 0x70, v171
	ds_write2st64_b64 v24, v[26:27], v[22:23] offset0:14 offset1:15
	v_mov_b32_e32 v22, 0xf0
	v_lshl_add_u32 v146, v164, 4, v22
	v_add_u32_e32 v22, s33, v146
	v_min_i32_e32 v22, 0x18698, v22
	v_ashrrev_i32_e32 v23, 31, v22
	v_lshlrev_b64 v[22:23], 11, v[22:23]
	v_lshl_add_u64 v[22:23], v[162:163], 0, v[22:23]
	s_movk_i32 s33, 0x1000
	v_add_co_u32_e64 v24, s[22:23], s33, v22
	s_movk_i32 s34, 0x2000
	s_nop 0
	v_addc_co_u32_e64 v25, s[22:23], 0, v23, s[22:23]
	v_add_co_u32_e64 v126, s[22:23], s34, v22
	s_movk_i32 s35, 0x3000
	s_nop 0
	v_addc_co_u32_e64 v127, s[22:23], 0, v23, s[22:23]
	global_load_dwordx4 v[122:125], v[22:23], off nt
	global_load_dwordx4 v[118:121], v[22:23], off offset:1024 nt
	global_load_dwordx4 v[102:105], v[22:23], off offset:2048 nt
	global_load_dwordx4 v[90:93], v[22:23], off offset:3072 nt
	v_add_co_u32_e64 v22, s[22:23], s35, v22
	global_load_dwordx4 v[106:109], v[24:25], off offset:1024 nt
	global_load_dwordx4 v[78:81], v[24:25], off offset:2048 nt
	global_load_dwordx4 v[74:77], v[126:127], off nt
	global_load_dwordx4 v[62:65], v[126:127], off offset:1024 nt
	global_load_dwordx4 v[58:61], v[126:127], off offset:2048 nt
	global_load_dwordx4 v[46:49], v[126:127], off offset:3072 nt
	v_addc_co_u32_e64 v23, s[22:23], 0, v23, s[22:23]
	global_load_dwordx4 v[110:113], v[24:25], off offset:3072 nt
	global_load_dwordx4 v[54:57], v[22:23], off nt
	global_load_dwordx4 v[30:33], v[22:23], off offset:1024 nt
	global_load_dwordx4 v[26:29], v[22:23], off offset:2048 nt
	s_nop 0
	global_load_dwordx4 v[126:129], v[126:127], off offset:-4096 nt
	s_nop 0
	global_load_dwordx4 v[22:25], v[22:23], off offset:3072 nt
	s_waitcnt vmcnt(40)
	v_cvt_pk_bf16_f32 v114, v114, v115
	v_cvt_pk_bf16_f32 v115, v116, v117
	s_waitcnt vmcnt(39)
	v_cvt_pk_bf16_f32 v94, v94, v95
	v_cvt_pk_bf16_f32 v95, v96, v97
	v_add_u32_e32 v96, 0x90, v171
	s_waitcnt vmcnt(34)
	v_cvt_pk_bf16_f32 v50, v50, v51
	v_cvt_pk_bf16_f32 v51, v52, v53
	s_waitcnt vmcnt(33)
	v_cvt_pk_bf16_f32 v38, v38, v39
	v_cvt_pk_bf16_f32 v39, v40, v41
	v_add_u32_e32 v40, 0xd0, v171
	v_cvt_pk_bf16_f32 v134, v138, v139
	v_cvt_pk_bf16_f32 v135, v140, v141
	v_cvt_pk_bf16_f32 v130, v130, v131
	v_cvt_pk_bf16_f32 v131, v132, v133
	v_add_u32_e32 v132, 0x80, v171
	ds_write2st64_b64 v96, v[114:115], v[94:95] offset0:18 offset1:19
	s_waitcnt vmcnt(28)
	v_cvt_pk_bf16_f32 v94, v142, v143
	v_cvt_pk_bf16_f32 v95, v144, v145
	v_cvt_pk_bf16_f32 v96, v98, v99
	v_cvt_pk_bf16_f32 v97, v100, v101
	v_add_u32_e32 v98, 0xa0, v171
	v_cvt_pk_bf16_f32 v82, v82, v83
	v_cvt_pk_bf16_f32 v83, v84, v85
	v_cvt_pk_bf16_f32 v84, v86, v87
	v_cvt_pk_bf16_f32 v85, v88, v89
	v_add_u32_e32 v86, 0xb0, v171
	v_cvt_pk_bf16_f32 v70, v70, v71
	v_cvt_pk_bf16_f32 v71, v72, v73
	v_cvt_pk_bf16_f32 v66, v66, v67
	v_cvt_pk_bf16_f32 v67, v68, v69
	v_add_u32_e32 v68, 0xc0, v171
	ds_write2st64_b64 v40, v[50:51], v[38:39] offset0:26 offset1:27
	v_cvt_pk_bf16_f32 v38, v42, v43
	v_cvt_pk_bf16_f32 v39, v44, v45
	v_cvt_pk_bf16_f32 v34, v34, v35
	v_cvt_pk_bf16_f32 v35, v36, v37
	v_add_u32_e32 v36, 0xe0, v171
	v_cvt_pk_bf16_f32 v18, v18, v19
	v_cvt_pk_bf16_f32 v19, v20, v21
	s_waitcnt vmcnt(27)
	v_cvt_pk_bf16_f32 v14, v14, v15
	v_cvt_pk_bf16_f32 v15, v16, v17
	v_add_u32_e32 v16, 0xf0, v171
	ds_write2st64_b64 v132, v[134:135], v[130:131] offset0:16 offset1:17
	ds_write2st64_b64 v98, v[94:95], v[96:97] offset0:20 offset1:21
	ds_write2st64_b64 v86, v[82:83], v[84:85] offset0:22 offset1:23
	ds_write2st64_b64 v68, v[70:71], v[66:67] offset0:24 offset1:25
	ds_write2st64_b64 v36, v[38:39], v[34:35] offset0:28 offset1:29
	ds_write2st64_b64 v16, v[18:19], v[14:15] offset0:30 offset1:31
	v_add_u32_e32 v14, s31, v146
	v_min_i32_e32 v14, 0x18698, v14
	v_ashrrev_i32_e32 v15, 31, v14
	v_lshlrev_b64 v[14:15], 11, v[14:15]
	v_lshl_add_u64 v[14:15], v[162:163], 0, v[14:15]
	v_add_co_u32_e64 v16, s[22:23], s33, v14
	global_load_dwordx4 v[138:141], v[14:15], off nt
	global_load_dwordx4 v[134:137], v[14:15], off offset:1024 nt
	global_load_dwordx4 v[130:133], v[14:15], off offset:2048 nt
	global_load_dwordx4 v[98:101], v[14:15], off offset:3072 nt
	v_addc_co_u32_e64 v17, s[22:23], 0, v15, s[22:23]
	v_add_co_u32_e64 v18, s[22:23], s34, v14
	s_nop 1
	v_addc_co_u32_e64 v19, s[22:23], 0, v15, s[22:23]
	v_add_co_u32_e64 v14, s[22:23], s35, v14
	global_load_dwordx4 v[114:117], v[16:17], off offset:1024 nt
	global_load_dwordx4 v[86:89], v[16:17], off offset:2048 nt
	global_load_dwordx4 v[82:85], v[18:19], off nt
	global_load_dwordx4 v[70:73], v[18:19], off offset:1024 nt
	global_load_dwordx4 v[66:69], v[18:19], off offset:2048 nt
	global_load_dwordx4 v[42:45], v[18:19], off offset:3072 nt
	v_addc_co_u32_e64 v15, s[22:23], 0, v15, s[22:23]
	global_load_dwordx4 v[94:97], v[16:17], off offset:3072 nt
	global_load_dwordx4 v[50:53], v[14:15], off nt
	global_load_dwordx4 v[38:41], v[14:15], off offset:1024 nt
	global_load_dwordx4 v[34:37], v[14:15], off offset:2048 nt
	global_load_dwordx4 v[142:145], v[18:19], off offset:-4096 nt
	s_nop 0
	global_load_dwordx4 v[18:21], v[14:15], off offset:3072 nt
	v_mov_b32_e32 v14, 0x14500
	v_lshl_add_u32 v147, v173, 4, v14
	ds_read_b128 v[14:17], v147
	ds_read_b128 v[174:177], v147 offset:1024
	ds_read_b128 v[178:181], v168
	ds_read_b128 v[182:185], v168 offset:16
	s_waitcnt lgkmcnt(1)
	v_mfma_f32_16x16x32_bf16 v[14:17], v[14:17], v[178:181], 0
	ds_read_b128 v[178:181], v147 offset:2048
	ds_read_b128 v[186:189], v147 offset:3072
	s_waitcnt lgkmcnt(2)
	v_mfma_f32_16x16x32_bf16 v[14:17], v[174:177], v[182:185], v[14:17]
	ds_read_b128 v[174:177], v168 offset:32
	ds_read_b128 v[182:185], v168 offset:48
	s_waitcnt lgkmcnt(1)
	v_mfma_f32_16x16x32_bf16 v[14:17], v[178:181], v[174:177], v[14:17]
	s_waitcnt lgkmcnt(0)
	v_mfma_f32_16x16x32_bf16 v[14:17], v[186:189], v[182:185], v[14:17]
	ds_read_b128 v[174:177], v147 offset:4096
	ds_read_b128 v[178:181], v147 offset:5120
	ds_read_b128 v[182:185], v168 offset:64
	ds_read_b128 v[186:189], v168 offset:80
	s_waitcnt lgkmcnt(1)
	v_mfma_f32_16x16x32_bf16 v[14:17], v[174:177], v[182:185], v[14:17]
	ds_read_b128 v[174:177], v147 offset:6144
	ds_read_b128 v[182:185], v147 offset:7168
	s_waitcnt lgkmcnt(2)
	v_mfma_f32_16x16x32_bf16 v[14:17], v[178:181], v[186:189], v[14:17]
	ds_read_b128 v[178:181], v168 offset:96
	ds_read_b128 v[186:189], v168 offset:112
	s_waitcnt lgkmcnt(1)
	v_mfma_f32_16x16x32_bf16 v[14:17], v[174:177], v[178:181], v[14:17]
	s_waitcnt lgkmcnt(0)
	v_mfma_f32_16x16x32_bf16 v[14:17], v[182:185], v[186:189], v[14:17]
	ds_read_b128 v[174:177], v147 offset:8192
	ds_read_b128 v[178:181], v147 offset:9216
	ds_read_b128 v[182:185], v168 offset:128
	ds_read_b128 v[186:189], v168 offset:144
	s_waitcnt lgkmcnt(1)
	v_mfma_f32_16x16x32_bf16 v[14:17], v[174:177], v[182:185], v[14:17]
	ds_read_b128 v[174:177], v147 offset:10240
	ds_read_b128 v[182:185], v147 offset:11264
	s_waitcnt lgkmcnt(2)
	v_mfma_f32_16x16x32_bf16 v[14:17], v[178:181], v[186:189], v[14:17]
	ds_read_b128 v[178:181], v168 offset:160
	ds_read_b128 v[186:189], v168 offset:176
	s_waitcnt lgkmcnt(1)
	v_mfma_f32_16x16x32_bf16 v[14:17], v[174:177], v[178:181], v[14:17]
	s_waitcnt lgkmcnt(0)
	v_mfma_f32_16x16x32_bf16 v[14:17], v[182:185], v[186:189], v[14:17]
	ds_read_b128 v[174:177], v147 offset:12288
	ds_read_b128 v[178:181], v147 offset:13312
	ds_read_b128 v[182:185], v168 offset:192
	ds_read_b128 v[186:189], v168 offset:208
	s_waitcnt lgkmcnt(1)
	v_mfma_f32_16x16x32_bf16 v[14:17], v[174:177], v[182:185], v[14:17]
	ds_read_b128 v[174:177], v147 offset:14336
	ds_read_b128 v[182:185], v147 offset:15360
	s_waitcnt lgkmcnt(2)
	v_mfma_f32_16x16x32_bf16 v[14:17], v[178:181], v[186:189], v[14:17]
	ds_read_b128 v[178:181], v168 offset:224
	ds_read_b128 v[186:189], v168 offset:240
	s_waitcnt lgkmcnt(1)
	v_mfma_f32_16x16x32_bf16 v[14:17], v[174:177], v[178:181], v[14:17]
	s_waitcnt lgkmcnt(0)
	v_mfma_f32_16x16x32_bf16 v[14:17], v[182:185], v[186:189], v[14:17]
	s_waitcnt vmcnt(42)
	v_cmp_ne_u16_e64 s[22:23], -1, v172
	s_and_b64 s[22:23], s[20:21], s[22:23]
	s_and_saveexec_b64 s[20:21], s[22:23]
	v_and_b32_e32 v147, 0xffff, v172
	v_mov_b32_e32 v148, 0x18500
	v_lshl_add_u32 v147, v147, 2, v148
	v_mov_b32_e32 v148, 1
	ds_add_u32 v147, v148
	s_or_b64 exec, exec, s[20:21]
	v_mov_b32_e32 v147, 0xffff
	s_mov_b32 s22, 0xffff
	s_waitcnt vmcnt(41)
	v_cndmask_b32_sdwa v148, v147, v161, vcc dst_sel:DWORD dst_unused:UNUSED_PAD src0_sel:DWORD src1_sel:WORD_0
	v_cmp_ne_u32_e32 vcc, s22, v148
	s_and_saveexec_b64 s[20:21], vcc
	v_mov_b32_e32 v149, 0x18500
	v_lshl_add_u32 v148, v148, 2, v149
	v_mov_b32_e32 v149, 1
	ds_add_u32 v148, v149
	s_or_b64 exec, exec, s[20:21]
	s_mov_b64 vcc, s[16:17]
	s_waitcnt vmcnt(40)
	v_cndmask_b32_sdwa v147, v147, v160, vcc dst_sel:DWORD dst_unused:UNUSED_PAD src0_sel:DWORD src1_sel:WORD_0
	v_cmp_ne_u32_e32 vcc, s22, v147
	s_and_saveexec_b64 s[16:17], vcc
	v_mov_b32_e32 v148, 0x18500
	v_lshl_add_u32 v147, v147, 2, v148
	v_mov_b32_e32 v148, 1
	ds_add_u32 v147, v148
	s_or_b64 exec, exec, s[16:17]
	s_mov_b64 vcc, s[18:19]
	v_mov_b32_e32 v147, 0xffff
	s_mov_b32 s18, 0xffff
	s_waitcnt vmcnt(39)
	v_cndmask_b32_sdwa v148, v147, v159, vcc dst_sel:DWORD dst_unused:UNUSED_PAD src0_sel:DWORD src1_sel:WORD_0
	v_cmp_ne_u32_e32 vcc, s18, v148
	s_and_saveexec_b64 s[16:17], vcc
	v_mov_b32_e32 v149, 0x18500
	v_lshl_add_u32 v148, v148, 2, v149
	v_mov_b32_e32 v149, 1
	ds_add_u32 v148, v149
	s_or_b64 exec, exec, s[16:17]
	s_mov_b64 vcc, s[12:13]
	s_waitcnt vmcnt(38)
	v_cndmask_b32_sdwa v147, v147, v157, vcc dst_sel:DWORD dst_unused:UNUSED_PAD src0_sel:DWORD src1_sel:WORD_0
	v_cmp_ne_u32_e32 vcc, s18, v147
	s_and_saveexec_b64 s[12:13], vcc
	v_mov_b32_e32 v148, 0x18500
	v_lshl_add_u32 v147, v147, 2, v148
	v_mov_b32_e32 v148, 1
	ds_add_u32 v147, v148
	s_or_b64 exec, exec, s[12:13]
	s_mov_b64 vcc, s[14:15]
	v_mov_b32_e32 v147, 0xffff
	s_mov_b32 s14, 0xffff
	s_waitcnt vmcnt(37)
	v_cndmask_b32_sdwa v148, v147, v156, vcc dst_sel:DWORD dst_unused:UNUSED_PAD src0_sel:DWORD src1_sel:WORD_0
	v_cmp_ne_u32_e32 vcc, s14, v148
	s_and_saveexec_b64 s[12:13], vcc
	v_mov_b32_e32 v149, 0x18500
	v_lshl_add_u32 v148, v148, 2, v149
	v_mov_b32_e32 v149, 1
	ds_add_u32 v148, v149
	s_or_b64 exec, exec, s[12:13]
	s_mov_b64 vcc, s[10:11]
	s_waitcnt vmcnt(36)
	v_cndmask_b32_sdwa v147, v147, v155, vcc dst_sel:DWORD dst_unused:UNUSED_PAD src0_sel:DWORD src1_sel:WORD_0
	v_cmp_ne_u32_e32 vcc, s14, v147
	s_and_saveexec_b64 s[10:11], vcc
	v_mov_b32_e32 v148, 0x18500
	v_lshl_add_u32 v147, v147, 2, v148
	v_mov_b32_e32 v148, 1
	ds_add_u32 v147, v148
	s_or_b64 exec, exec, s[10:11]
	s_mov_b64 vcc, s[4:5]
	v_mov_b32_e32 v147, 0xffff
	s_mov_b32 s10, 0xffff
	s_waitcnt vmcnt(35)
	v_cndmask_b32_sdwa v148, v147, v153, vcc dst_sel:DWORD dst_unused:UNUSED_PAD src0_sel:DWORD src1_sel:WORD_0
	v_cmp_ne_u32_e32 vcc, s10, v148
	s_and_saveexec_b64 s[4:5], vcc
	v_mov_b32_e32 v149, 0x18500
	v_lshl_add_u32 v148, v148, 2, v149
	v_mov_b32_e32 v149, 1
	ds_add_u32 v148, v149
	s_or_b64 exec, exec, s[4:5]
	s_mov_b64 vcc, s[6:7]
	s_waitcnt vmcnt(34)
	v_cndmask_b32_sdwa v147, v147, v154, vcc dst_sel:DWORD dst_unused:UNUSED_PAD src0_sel:DWORD src1_sel:WORD_0
	v_cmp_ne_u32_e32 vcc, s10, v147
	s_and_saveexec_b64 s[4:5], vcc
	v_mov_b32_e32 v148, 0x18500
	v_lshl_add_u32 v147, v147, 2, v148
	v_mov_b32_e32 v148, 1
	ds_add_u32 v147, v148
	s_or_b64 exec, exec, s[4:5]
	s_mov_b64 vcc, s[8:9]
	v_mov_b32_e32 v147, 0xffff
	s_mov_b32 s6, 0xffff
	s_waitcnt vmcnt(33)
	v_cndmask_b32_sdwa v148, v147, v152, vcc dst_sel:DWORD dst_unused:UNUSED_PAD src0_sel:DWORD src1_sel:WORD_0
	v_cmp_ne_u32_e32 vcc, s6, v148
	s_and_saveexec_b64 s[4:5], vcc
	v_mov_b32_e32 v149, 0x18500
	v_lshl_add_u32 v148, v148, 2, v149
	v_mov_b32_e32 v149, 1
	ds_add_u32 v148, v149
	s_or_b64 exec, exec, s[4:5]
	s_mov_b64 vcc, s[0:1]
	s_waitcnt vmcnt(32)
	v_cndmask_b32_sdwa v147, v147, v151, vcc dst_sel:DWORD dst_unused:UNUSED_PAD src0_sel:DWORD src1_sel:WORD_0
	v_cmp_ne_u32_e32 vcc, s6, v147
	s_and_saveexec_b64 s[0:1], vcc
	v_mov_b32_e32 v148, 0x18500
	v_lshl_add_u32 v147, v147, 2, v148
	v_mov_b32_e32 v148, 1
	ds_add_u32 v147, v148
	s_or_b64 exec, exec, s[0:1]
	v_mov_b32_e32 v184, v1
	ds_read2_b32 v[148:149], v169 offset0:220 offset1:225
	ds_read2_b32 v[152:153], v170 offset0:220 offset1:225
	ds_read2_b32 v[154:155], v170 offset0:230 offset1:235
	ds_read2_b32 v[156:157], v169 offset0:230 offset1:235
	v_mov_b32_e32 v161, 0
	s_waitcnt lgkmcnt(3)
	v_add_u32_e32 v147, v148, v1
	s_waitcnt lgkmcnt(2)
	v_cmp_lt_u32_e64 s[20:21], v1, v152
	v_cmp_lt_u32_e32 vcc, v1, v153
	s_waitcnt lgkmcnt(1)
	v_cmp_lt_u32_e64 s[16:17], v1, v154
	v_cndmask_b32_e64 v160, 0, v147, s[20:21]
	v_add_u32_e32 v147, v149, v1
	v_lshl_add_u64 v[162:163], v[160:161], 1, s[26:27]
	v_cndmask_b32_e32 v160, 0, v147, vcc
	s_waitcnt lgkmcnt(0)
	v_add_u32_e32 v147, v156, v1
	v_lshl_add_u64 v[148:149], v[160:161], 1, s[26:27]
	v_cndmask_b32_e64 v160, 0, v147, s[16:17]
	v_add_u32_e32 v147, v157, v1
	ds_read2_b32 v[156:157], v169 offset0:240 offset1:245
	ds_read2_b32 v[172:173], v170 offset0:240 offset1:245
	v_cmp_lt_u32_e64 s[18:19], v1, v155
	v_lshl_add_u64 v[152:153], v[160:161], 1, s[26:27]
	s_waitcnt lgkmcnt(0)
	v_cmp_lt_u32_e64 s[12:13], v1, v172
	v_cndmask_b32_e64 v160, 0, v147, s[18:19]
	v_add_u32_e32 v147, v156, v1
	v_lshl_add_u64 v[154:155], v[160:161], 1, s[26:27]
	v_cndmask_b32_e64 v160, 0, v147, s[12:13]
	v_add_u32_e32 v147, v157, v1
	ds_read2_b32 v[156:157], v169 offset0:250 offset1:255
	ds_read2_b32 v[176:177], v170 offset0:250 offset1:255
	v_cmp_lt_u32_e64 s[14:15], v1, v173
	v_lshl_add_u64 v[174:175], v[160:161], 1, s[26:27]
	s_waitcnt lgkmcnt(0)
	v_cmp_lt_u32_e64 s[10:11], v1, v176
	v_cndmask_b32_e64 v160, 0, v147, s[14:15]
	v_add_u32_e32 v147, v156, v1
	v_lshl_add_u64 v[172:173], v[160:161], 1, s[26:27]
	v_cndmask_b32_e64 v160, 0, v147, s[10:11]
	v_add_u32_e32 v147, v157, v1
	v_cmp_lt_u32_e64 s[4:5], v1, v177
	v_lshl_add_u64 v[178:179], v[160:161], 1, s[26:27]
	s_nop 0
	v_cndmask_b32_e64 v160, 0, v147, s[4:5]
	v_add_u32_e32 v147, 0x400, v169
	ds_read2_b32 v[180:181], v147 offset0:4 offset1:9
	v_add_u32_e32 v147, 0x400, v170
	ds_read2_b32 v[182:183], v147 offset0:4 offset1:9
	v_lshl_add_u64 v[176:177], v[160:161], 1, s[26:27]
	global_load_ushort v159, v[162:163], off
	global_load_ushort v157, v[148:149], off
	global_load_ushort v156, v[152:153], off
	s_nop 0
	global_load_ushort v155, v[154:155], off
	s_nop 0
	global_load_ushort v154, v[174:175], off
	global_load_ushort v153, v[172:173], off
	global_load_ushort v152, v[178:179], off
	global_load_ushort v149, v[176:177], off
	ds_read_b32 v148, v169 offset:1080
	ds_read_b32 v151, v170 offset:1080
	s_waitcnt lgkmcnt(3)
	v_add_u32_e32 v147, v180, v1
	s_waitcnt lgkmcnt(2)
	v_cmp_lt_u32_e64 s[6:7], v1, v182
	v_cmp_lt_u32_e64 s[8:9], v1, v183
	s_waitcnt lgkmcnt(0)
	v_cmp_lt_u32_e64 s[0:1], v1, v151
	v_cndmask_b32_e64 v160, 0, v147, s[6:7]
	v_add_u32_e32 v147, v181, v1
	v_lshl_add_u64 v[162:163], v[160:161], 1, s[26:27]
	v_cndmask_b32_e64 v160, 0, v147, s[8:9]
	v_add_u32_e32 v147, v148, v1
	v_lshl_add_u64 v[172:173], v[160:161], 1, s[26:27]
	v_cndmask_b32_e64 v160, 0, v147, s[0:1]
	v_lshl_add_u64 v[160:161], v[160:161], 1, s[26:27]
	global_load_ushort v151, v[162:163], off
	global_load_ushort v148, v[172:173], off
	global_load_ushort v147, v[160:161], off
	s_waitcnt vmcnt(40)
	v_cvt_pk_bf16_f32 v102, v102, v103
	v_cvt_pk_bf16_f32 v103, v104, v105
	s_waitcnt vmcnt(39)
	v_cvt_pk_bf16_f32 v90, v90, v91
	v_cvt_pk_bf16_f32 v91, v92, v93
	ds_write2_b64 v171, v[102:103], v[90:91] offset0:130 offset1:194
	s_waitcnt vmcnt(28)
	v_cvt_pk_bf16_f32 v90, v126, v127
	v_cvt_pk_bf16_f32 v91, v128, v129
	v_cvt_pk_bf16_f32 v92, v106, v107
	v_cvt_pk_bf16_f32 v93, v108, v109
	v_add_u32_e32 v102, 32, v171
	v_cvt_pk_bf16_f32 v58, v58, v59
	v_cvt_pk_bf16_f32 v59, v60, v61
	v_cvt_pk_bf16_f32 v46, v46, v47
	v_cvt_pk_bf16_f32 v47, v48, v49
	v_add_u32_e32 v48, 0x50, v171
	v_cvt_pk_bf16_f32 v122, v122, v123
	v_cvt_pk_bf16_f32 v123, v124, v125
	v_cvt_pk_bf16_f32 v118, v118, v119
	v_cvt_pk_bf16_f32 v119, v120, v121
	ds_write2st64_b64 v102, v[90:91], v[92:93] offset0:4 offset1:5
	v_cvt_pk_bf16_f32 v78, v78, v79
	v_cvt_pk_bf16_f32 v79, v80, v81
	v_cvt_pk_bf16_f32 v80, v110, v111
	v_cvt_pk_bf16_f32 v81, v112, v113
	v_add_u32_e32 v90, 48, v171
	v_cvt_pk_bf16_f32 v74, v74, v75
	v_cvt_pk_bf16_f32 v75, v76, v77
	v_cvt_pk_bf16_f32 v62, v62, v63
	v_cvt_pk_bf16_f32 v63, v64, v65
	v_add_u32_e32 v64, 64, v171
	ds_write2st64_b64 v48, v[58:59], v[46:47] offset0:10 offset1:11
	v_cvt_pk_bf16_f32 v46, v54, v55
	v_cvt_pk_bf16_f32 v47, v56, v57
	v_cvt_pk_bf16_f32 v30, v30, v31
	v_cvt_pk_bf16_f32 v31, v32, v33
	v_add_u32_e32 v32, 0x60, v171
	v_cvt_pk_bf16_f32 v26, v26, v27
	v_cvt_pk_bf16_f32 v27, v28, v29
	s_waitcnt vmcnt(27)
	v_cvt_pk_bf16_f32 v22, v22, v23
	v_cvt_pk_bf16_f32 v23, v24, v25
	v_add_u32_e32 v24, 0x70, v171
	ds_write2st64_b64 v171, v[122:123], v[118:119] offset1:1
	ds_write2st64_b64 v90, v[78:79], v[80:81] offset0:6 offset1:7
	ds_write2st64_b64 v64, v[74:75], v[62:63] offset0:8 offset1:9
	ds_write2st64_b64 v32, v[46:47], v[30:31] offset0:12 offset1:13
	ds_write2st64_b64 v24, v[26:27], v[22:23] offset0:14 offset1:15
	s_waitcnt vmcnt(26)
	v_cvt_pk_bf16_f32 v22, v138, v139
	v_cvt_pk_bf16_f32 v23, v140, v141
	s_waitcnt vmcnt(25)
	v_cvt_pk_bf16_f32 v24, v134, v135
	v_cvt_pk_bf16_f32 v25, v136, v137
	v_add_u32_e32 v26, 0x80, v171
	ds_write2st64_b64 v26, v[22:23], v[24:25] offset0:16 offset1:17
	s_waitcnt vmcnt(24)
	v_cvt_pk_bf16_f32 v22, v130, v131
	v_cvt_pk_bf16_f32 v23, v132, v133
	s_waitcnt vmcnt(23)
	v_cvt_pk_bf16_f32 v24, v98, v99
	v_cvt_pk_bf16_f32 v25, v100, v101
	v_add_u32_e32 v26, 0x90, v171
	ds_write2st64_b64 v26, v[22:23], v[24:25] offset0:18 offset1:19
	s_waitcnt vmcnt(12)
	v_cvt_pk_bf16_f32 v22, v142, v143
	v_cvt_pk_bf16_f32 v23, v144, v145
	v_cvt_pk_bf16_f32 v24, v114, v115
	v_cvt_pk_bf16_f32 v25, v116, v117
	v_add_u32_e32 v26, 0xa0, v171
	ds_write2st64_b64 v26, v[22:23], v[24:25] offset0:20 offset1:21
	v_cvt_pk_bf16_f32 v22, v86, v87
	v_cvt_pk_bf16_f32 v23, v88, v89
	v_cvt_pk_bf16_f32 v24, v94, v95
	v_cvt_pk_bf16_f32 v25, v96, v97
	v_add_u32_e32 v26, 0xb0, v171
	ds_write2st64_b64 v26, v[22:23], v[24:25] offset0:22 offset1:23
	v_cvt_pk_bf16_f32 v22, v82, v83
	v_cvt_pk_bf16_f32 v23, v84, v85
	v_cvt_pk_bf16_f32 v24, v70, v71
	v_cvt_pk_bf16_f32 v25, v72, v73
	v_add_u32_e32 v26, 0xc0, v171
	ds_write2st64_b64 v26, v[22:23], v[24:25] offset0:24 offset1:25
	v_cvt_pk_bf16_f32 v22, v66, v67
	v_cvt_pk_bf16_f32 v23, v68, v69
	v_cvt_pk_bf16_f32 v24, v42, v43
	v_cvt_pk_bf16_f32 v25, v44, v45
	v_add_u32_e32 v26, 0xd0, v171
	ds_write2st64_b64 v26, v[22:23], v[24:25] offset0:26 offset1:27
	v_cvt_pk_bf16_f32 v22, v50, v51
	v_cvt_pk_bf16_f32 v23, v52, v53
	v_cvt_pk_bf16_f32 v24, v38, v39
	v_cvt_pk_bf16_f32 v25, v40, v41
	v_add_u32_e32 v26, 0xe0, v171
	ds_write2st64_b64 v26, v[22:23], v[24:25] offset0:28 offset1:29
	v_cvt_pk_bf16_f32 v22, v34, v35
	v_cvt_pk_bf16_f32 v23, v36, v37
	s_waitcnt vmcnt(11)
	v_cvt_pk_bf16_f32 v18, v18, v19
	v_cvt_pk_bf16_f32 v19, v20, v21
	v_add_u32_e32 v20, 0xf0, v171
	ds_write2st64_b64 v20, v[22:23], v[18:19] offset0:30 offset1:31
	v_mov_b32_e32 v18, 0x14500
	v_lshl_add_u32 v38, v184, 4, v18
	ds_read_b128 v[18:21], v38
	ds_read_b128 v[22:25], v38 offset:1024
	ds_read_b128 v[26:29], v168
	ds_read_b128 v[30:33], v168 offset:16
	s_waitcnt lgkmcnt(1)
	v_mfma_f32_16x16x32_bf16 v[18:21], v[18:21], v[26:29], 0
	ds_read_b128 v[26:29], v38 offset:2048
	ds_read_b128 v[34:37], v38 offset:3072
	s_waitcnt lgkmcnt(2)
	v_mfma_f32_16x16x32_bf16 v[18:21], v[22:25], v[30:33], v[18:21]
	ds_read_b128 v[22:25], v168 offset:32
	ds_read_b128 v[30:33], v168 offset:48
	s_waitcnt lgkmcnt(1)
	v_mfma_f32_16x16x32_bf16 v[18:21], v[26:29], v[22:25], v[18:21]
	s_waitcnt lgkmcnt(0)
	v_mfma_f32_16x16x32_bf16 v[18:21], v[34:37], v[30:33], v[18:21]
	ds_read_b128 v[22:25], v38 offset:4096
	ds_read_b128 v[26:29], v38 offset:5120
	ds_read_b128 v[30:33], v168 offset:64
	ds_read_b128 v[34:37], v168 offset:80
	s_waitcnt lgkmcnt(1)
	v_mfma_f32_16x16x32_bf16 v[18:21], v[22:25], v[30:33], v[18:21]
	ds_read_b128 v[22:25], v38 offset:6144
	ds_read_b128 v[30:33], v38 offset:7168
	s_waitcnt lgkmcnt(2)
	v_mfma_f32_16x16x32_bf16 v[18:21], v[26:29], v[34:37], v[18:21]
	ds_read_b128 v[26:29], v168 offset:96
	ds_read_b128 v[34:37], v168 offset:112
	s_waitcnt lgkmcnt(1)
	v_mfma_f32_16x16x32_bf16 v[18:21], v[22:25], v[26:29], v[18:21]
	s_waitcnt lgkmcnt(0)
	v_mfma_f32_16x16x32_bf16 v[18:21], v[30:33], v[34:37], v[18:21]
	ds_read_b128 v[22:25], v38 offset:8192
	ds_read_b128 v[26:29], v38 offset:9216
	ds_read_b128 v[30:33], v168 offset:128
	ds_read_b128 v[34:37], v168 offset:144
	s_waitcnt lgkmcnt(1)
	v_mfma_f32_16x16x32_bf16 v[18:21], v[22:25], v[30:33], v[18:21]
	ds_read_b128 v[22:25], v38 offset:10240
	ds_read_b128 v[30:33], v38 offset:11264
	s_waitcnt lgkmcnt(2)
	v_mfma_f32_16x16x32_bf16 v[18:21], v[26:29], v[34:37], v[18:21]
	ds_read_b128 v[26:29], v168 offset:160
	ds_read_b128 v[34:37], v168 offset:176
	s_waitcnt lgkmcnt(1)
	v_mfma_f32_16x16x32_bf16 v[18:21], v[22:25], v[26:29], v[18:21]
	s_waitcnt lgkmcnt(0)
	v_mfma_f32_16x16x32_bf16 v[18:21], v[30:33], v[34:37], v[18:21]
	ds_read_b128 v[22:25], v38 offset:12288
	ds_read_b128 v[26:29], v38 offset:13312
	ds_read_b128 v[30:33], v168 offset:192
	ds_read_b128 v[34:37], v168 offset:208
	s_waitcnt lgkmcnt(1)
	v_mfma_f32_16x16x32_bf16 v[18:21], v[22:25], v[30:33], v[18:21]
	ds_read_b128 v[22:25], v38 offset:14336
	ds_read_b128 v[30:33], v38 offset:15360
	s_waitcnt lgkmcnt(2)
	v_mfma_f32_16x16x32_bf16 v[18:21], v[26:29], v[34:37], v[18:21]
	ds_read_b128 v[26:29], v168 offset:224
	ds_read_b128 v[34:37], v168 offset:240
	s_waitcnt lgkmcnt(1)
	v_mfma_f32_16x16x32_bf16 v[18:21], v[22:25], v[26:29], v[18:21]
	s_waitcnt lgkmcnt(0)
	v_mfma_f32_16x16x32_bf16 v[18:21], v[30:33], v[34:37], v[18:21]
	s_waitcnt vmcnt(10)
	v_cmp_ne_u16_e64 s[22:23], -1, v159
	s_and_b64 s[22:23], s[20:21], s[22:23]
	s_and_saveexec_b64 s[20:21], s[22:23]
	v_and_b32_e32 v22, 0xffff, v159
	v_mov_b32_e32 v23, 0x18500
	v_lshl_add_u32 v22, v22, 2, v23
	v_mov_b32_e32 v23, 1
	ds_add_u32 v22, v23
	s_or_b64 exec, exec, s[20:21]
	v_mov_b32_e32 v22, 0xffff
	s_mov_b32 s22, 0xffff
	s_waitcnt vmcnt(9)
	v_cndmask_b32_sdwa v23, v22, v157, vcc dst_sel:DWORD dst_unused:UNUSED_PAD src0_sel:DWORD src1_sel:WORD_0
	v_cmp_ne_u32_e32 vcc, s22, v23
	s_and_saveexec_b64 s[20:21], vcc
	v_mov_b32_e32 v24, 0x18500
	v_lshl_add_u32 v23, v23, 2, v24
	v_mov_b32_e32 v24, 1
	ds_add_u32 v23, v24
	s_or_b64 exec, exec, s[20:21]
	s_mov_b64 vcc, s[16:17]
	s_waitcnt vmcnt(8)
	v_cndmask_b32_sdwa v22, v22, v156, vcc dst_sel:DWORD dst_unused:UNUSED_PAD src0_sel:DWORD src1_sel:WORD_0
	v_cmp_ne_u32_e32 vcc, s22, v22
	s_and_saveexec_b64 s[16:17], vcc
	v_mov_b32_e32 v23, 0x18500
	v_lshl_add_u32 v22, v22, 2, v23
	v_mov_b32_e32 v23, 1
	ds_add_u32 v22, v23
	s_or_b64 exec, exec, s[16:17]
	s_mov_b64 vcc, s[18:19]
	v_mov_b32_e32 v22, 0xffff
	s_mov_b32 s18, 0xffff
	s_waitcnt vmcnt(7)
	v_cndmask_b32_sdwa v23, v22, v155, vcc dst_sel:DWORD dst_unused:UNUSED_PAD src0_sel:DWORD src1_sel:WORD_0
	v_cmp_ne_u32_e32 vcc, s18, v23
	s_and_saveexec_b64 s[16:17], vcc
	v_mov_b32_e32 v24, 0x18500
	v_lshl_add_u32 v23, v23, 2, v24
	v_mov_b32_e32 v24, 1
	ds_add_u32 v23, v24
	s_or_b64 exec, exec, s[16:17]
	s_mov_b64 vcc, s[12:13]
	s_waitcnt vmcnt(6)
	v_cndmask_b32_sdwa v22, v22, v154, vcc dst_sel:DWORD dst_unused:UNUSED_PAD src0_sel:DWORD src1_sel:WORD_0
	v_cmp_ne_u32_e32 vcc, s18, v22
	s_and_saveexec_b64 s[12:13], vcc
	v_mov_b32_e32 v23, 0x18500
	v_lshl_add_u32 v22, v22, 2, v23
	v_mov_b32_e32 v23, 1
	ds_add_u32 v22, v23
	s_or_b64 exec, exec, s[12:13]
	s_mov_b64 vcc, s[14:15]
	v_mov_b32_e32 v22, 0xffff
	s_mov_b32 s14, 0xffff
	s_waitcnt vmcnt(5)
	v_cndmask_b32_sdwa v23, v22, v153, vcc dst_sel:DWORD dst_unused:UNUSED_PAD src0_sel:DWORD src1_sel:WORD_0
	v_cmp_ne_u32_e32 vcc, s14, v23
	s_and_saveexec_b64 s[12:13], vcc
	v_mov_b32_e32 v24, 0x18500
	v_lshl_add_u32 v23, v23, 2, v24
	v_mov_b32_e32 v24, 1
	ds_add_u32 v23, v24
	s_or_b64 exec, exec, s[12:13]
	s_mov_b64 vcc, s[10:11]
	s_waitcnt vmcnt(4)
	v_cndmask_b32_sdwa v22, v22, v152, vcc dst_sel:DWORD dst_unused:UNUSED_PAD src0_sel:DWORD src1_sel:WORD_0
	v_cmp_ne_u32_e32 vcc, s14, v22
	s_and_saveexec_b64 s[10:11], vcc
	v_mov_b32_e32 v23, 0x18500
	v_lshl_add_u32 v22, v22, 2, v23
	v_mov_b32_e32 v23, 1
	ds_add_u32 v22, v23
	s_or_b64 exec, exec, s[10:11]
	s_mov_b64 vcc, s[4:5]
	v_mov_b32_e32 v22, 0xffff
	s_mov_b32 s10, 0xffff
	s_waitcnt vmcnt(3)
	v_cndmask_b32_sdwa v23, v22, v149, vcc dst_sel:DWORD dst_unused:UNUSED_PAD src0_sel:DWORD src1_sel:WORD_0
	v_cmp_ne_u32_e32 vcc, s10, v23
	s_and_saveexec_b64 s[4:5], vcc
	v_mov_b32_e32 v24, 0x18500
	v_lshl_add_u32 v23, v23, 2, v24
	v_mov_b32_e32 v24, 1
	ds_add_u32 v23, v24
	s_or_b64 exec, exec, s[4:5]
	s_mov_b64 vcc, s[6:7]
	s_waitcnt vmcnt(2)
	v_cndmask_b32_sdwa v22, v22, v151, vcc dst_sel:DWORD dst_unused:UNUSED_PAD src0_sel:DWORD src1_sel:WORD_0
	v_cmp_ne_u32_e32 vcc, s10, v22
	s_and_saveexec_b64 s[4:5], vcc
	v_mov_b32_e32 v23, 0x18500
	v_lshl_add_u32 v22, v22, 2, v23
	v_mov_b32_e32 v23, 1
	ds_add_u32 v22, v23
	s_or_b64 exec, exec, s[4:5]
	s_mov_b64 vcc, s[8:9]
	v_mov_b32_e32 v22, 0xffff
	s_mov_b32 s6, 0xffff
	s_waitcnt vmcnt(1)
	v_cndmask_b32_sdwa v23, v22, v148, vcc dst_sel:DWORD dst_unused:UNUSED_PAD src0_sel:DWORD src1_sel:WORD_0
	v_cmp_ne_u32_e32 vcc, s6, v23
	s_and_saveexec_b64 s[4:5], vcc
	v_mov_b32_e32 v24, 0x18500
	v_lshl_add_u32 v23, v23, 2, v24
	v_mov_b32_e32 v24, 1
	ds_add_u32 v23, v24
	s_or_b64 exec, exec, s[4:5]
	s_mov_b64 vcc, s[0:1]
	s_waitcnt vmcnt(0)
	v_cndmask_b32_sdwa v22, v22, v147, vcc dst_sel:DWORD dst_unused:UNUSED_PAD src0_sel:DWORD src1_sel:WORD_0
	v_cmp_ne_u32_e32 vcc, s6, v22
	s_and_saveexec_b64 s[0:1], vcc
	v_mov_b32_e32 v23, 0x18500
	v_lshl_add_u32 v22, v22, 2, v23
	v_mov_b32_e32 v23, 1
	ds_add_u32 v22, v23
	s_or_b64 exec, exec, s[0:1]
	v_mbcnt_lo_u32_b32 v22, -1, 0
	v_mbcnt_hi_u32_b32 v22, -1, v22
	v_mad_u32_u24 v23, v22, 5, v164
	s_mov_b64 s[40:41], exec
	s_movk_i32 s44, 0x100
	v_cmp_gt_u32_e32 vcc, s44, v23
	s_and_b64 exec, s[40:41], vcc
	v_lshlrev_b32_e32 v23, 2, v23
	v_add_u32_e32 v24, 0x18b40, v23
	v_add_u32_e32 v25, 0x18fc0, v23
	ds_read_b32 v26, v24
	ds_read_b32 v27, v25
	s_waitcnt lgkmcnt(0)
	v_cmp_lt_u32_e32 vcc, 64, v26
	s_mov_b64 s[42:43], vcc
	s_mov_b64 exec, s[40:41]
	v_or_b32_e32 v28, 64, v22
	v_lshlrev_b32_e32 v29, 1, v22
	v_mov_b32_e32 v35, 1
.Lk2t_loop:
	s_cmp_eq_u64 s[42:43], 0
	s_cbranch_scc1 .Lk2t_done
	s_mov_b64 s[46:47], 0
	s_mov_b64 s[48:49], 0
	s_mov_b64 s[50:51], 0
	s_mov_b64 s[52:53], 0
	s_ff1_i32_b64 s44, s[42:43]
	v_readlane_b32 s45, v26, s44
	v_readlane_b32 s54, v27, s44
	s_bitset0_b64 s[42:43], s44
	s_nop 0
	v_cmp_gt_u32_e64 s[46:47], s45, v28
	s_add_i32 s54, s54, 64
	s_lshl_b32 s54, s54, 1
	s_add_u32 s56, s26, s54
	s_addc_u32 s57, s27, 0
	s_mov_b64 exec, s[46:47]
	global_load_ushort v30, v29, s[56:57]
	s_mov_b64 exec, s[40:41]
	s_cmp_eq_u64 s[42:43], 0
	s_cbranch_scc1 .Lk2t_proc
	s_ff1_i32_b64 s44, s[42:43]
	v_readlane_b32 s45, v26, s44
	v_readlane_b32 s54, v27, s44
	s_bitset0_b64 s[42:43], s44
	s_nop 0
	v_cmp_gt_u32_e64 s[48:49], s45, v28
	s_add_i32 s54, s54, 64
	s_lshl_b32 s54, s54, 1
	s_add_u32 s58, s26, s54
	s_addc_u32 s59, s27, 0
	s_mov_b64 exec, s[48:49]
	global_load_ushort v31, v29, s[58:59]
	s_mov_b64 exec, s[40:41]
	s_cmp_eq_u64 s[42:43], 0
	s_cbranch_scc1 .Lk2t_proc
	s_ff1_i32_b64 s44, s[42:43]
	v_readlane_b32 s45, v26, s44
	v_readlane_b32 s54, v27, s44
	s_bitset0_b64 s[42:43], s44
	s_nop 0
	v_cmp_gt_u32_e64 s[50:51], s45, v28
	s_add_i32 s54, s54, 64
	s_lshl_b32 s54, s54, 1
	s_add_u32 s60, s26, s54
	s_addc_u32 s61, s27, 0
	s_mov_b64 exec, s[50:51]
	global_load_ushort v32, v29, s[60:61]
	s_mov_b64 exec, s[40:41]
	s_cmp_eq_u64 s[42:43], 0
	s_cbranch_scc1 .Lk2t_proc
	s_ff1_i32_b64 s44, s[42:43]
	v_readlane_b32 s45, v26, s44
	v_readlane_b32 s54, v27, s44
	s_bitset0_b64 s[42:43], s44
	s_nop 0
	v_cmp_gt_u32_e64 s[52:53], s45, v28
	s_add_i32 s54, s54, 64
	s_lshl_b32 s54, s54, 1
	s_add_u32 s62, s26, s54
	s_addc_u32 s63, s27, 0
	s_mov_b64 exec, s[52:53]
	global_load_ushort v33, v29, s[62:63]
	s_mov_b64 exec, s[40:41]
.Lk2t_proc:
	s_waitcnt vmcnt(0)
	s_mov_b64 exec, s[46:47]
	v_lshlrev_b32_e32 v34, 2, v30
	v_add_u32_e32 v34, 0x18500, v34
	ds_add_u32 v34, v35
	s_mov_b64 exec, s[48:49]
	v_lshlrev_b32_e32 v34, 2, v31
	v_add_u32_e32 v34, 0x18500, v34
	ds_add_u32 v34, v35
	s_mov_b64 exec, s[50:51]
	v_lshlrev_b32_e32 v34, 2, v32
	v_add_u32_e32 v34, 0x18500, v34
	ds_add_u32 v34, v35
	s_mov_b64 exec, s[52:53]
	v_lshlrev_b32_e32 v34, 2, v33
	v_add_u32_e32 v34, 0x18500, v34
	ds_add_u32 v34, v35
	s_mov_b64 exec, s[40:41]
	s_branch .Lk2t_loop
.Lk2t_done:
	v_mov_b32_e32 v22, 0x19440
	s_waitcnt lgkmcnt(0)
	s_barrier
	ds_read_b32 v22, v22
	s_waitcnt lgkmcnt(0)
	v_cmp_ne_u32_e32 vcc, 0, v22
	s_cbranch_vccz .LBB1_162
	v_or_b32_e32 v1, 0x80, v1
	s_mov_b64 s[0:1], 0
	v_mov_b32_e32 v24, 0x18b40
	v_mov_b32_e32 v23, 0
	v_mov_b32_e32 v25, 1
	s_movk_i32 s8, 0xfa
	v_mov_b32_e32 v26, 0x18fc0
	v_mov_b32_e32 v27, 0x18500
	v_mov_b32_e32 v28, v164
	s_branch .LBB1_158

.LBB2_17:
	s_or_b64 exec, exec, s[38:39]
	s_mov_b64 s[2:3], exec
	v_mov_b32_e32 v100, 1
	s_waitcnt vmcnt(15)
	v_cndmask_b32_e64 v19, -1, v18, s[20:21]
	v_mul_u32_u24_e32 v18, 0x640, v6
	v_or_b32_e32 v18, 0x10000, v18
	s_and_b64 exec, s[2:3], s[20:21]
	v_lshrrev_b32_e32 v84, 15, v19
	v_and_b32_e32 v84, 0x1fffc, v84
	v_add_u32_e32 v84, v18, v84
	ds_add_u32 v84, v100
	s_mov_b64 exec, s[2:3]
	s_waitcnt vmcnt(14)
	v_cndmask_b32_e64 v20, -1, v16, s[8:9]
	s_and_b64 exec, s[2:3], s[8:9]
	v_lshrrev_b32_e32 v85, 15, v20
	v_and_b32_e32 v85, 0x1fffc, v85
	v_add_u32_e32 v85, v18, v85
	ds_add_u32 v85, v100
	s_mov_b64 exec, s[2:3]
	s_waitcnt vmcnt(13)
	v_cndmask_b32_e64 v21, -1, v14, s[10:11]
	s_and_b64 exec, s[2:3], s[10:11]
	v_lshrrev_b32_e32 v86, 15, v21
	v_and_b32_e32 v86, 0x1fffc, v86
	v_add_u32_e32 v86, v18, v86
	ds_add_u32 v86, v100
	s_mov_b64 exec, s[2:3]
	s_waitcnt vmcnt(12)
	v_cndmask_b32_e64 v22, -1, v13, s[12:13]
	s_and_b64 exec, s[2:3], s[12:13]
	v_lshrrev_b32_e32 v87, 15, v22
	v_and_b32_e32 v87, 0x1fffc, v87
	v_add_u32_e32 v87, v18, v87
	ds_add_u32 v87, v100
	s_mov_b64 exec, s[2:3]
	s_waitcnt vmcnt(11)
	v_cndmask_b32_e64 v23, -1, v11, s[14:15]
	s_and_b64 exec, s[2:3], s[14:15]
	v_lshrrev_b32_e32 v88, 15, v23
	v_and_b32_e32 v88, 0x1fffc, v88
	v_add_u32_e32 v88, v18, v88
	ds_add_u32 v88, v100
	s_mov_b64 exec, s[2:3]
	s_waitcnt vmcnt(10)
	v_cndmask_b32_e64 v24, -1, v9, s[16:17]
	s_and_b64 exec, s[2:3], s[16:17]
	v_lshrrev_b32_e32 v89, 15, v24
	v_and_b32_e32 v89, 0x1fffc, v89
	v_add_u32_e32 v89, v18, v89
	ds_add_u32 v89, v100
	s_mov_b64 exec, s[2:3]
	s_waitcnt vmcnt(9)
	v_cndmask_b32_e64 v25, -1, v8, s[18:19]
	s_and_b64 exec, s[2:3], s[18:19]
	v_lshrrev_b32_e32 v90, 15, v25
	v_and_b32_e32 v90, 0x1fffc, v90
	v_add_u32_e32 v90, v18, v90
	ds_add_u32 v90, v100
	s_mov_b64 exec, s[2:3]
	s_waitcnt vmcnt(8)
	v_cndmask_b32_e64 v26, -1, v7, s[22:23]
	s_and_b64 exec, s[2:3], s[22:23]
	v_lshrrev_b32_e32 v91, 15, v26
	v_and_b32_e32 v91, 0x1fffc, v91
	v_add_u32_e32 v91, v18, v91
	ds_add_u32 v91, v100
	s_mov_b64 exec, s[2:3]
	s_waitcnt vmcnt(7)
	v_cndmask_b32_e64 v27, -1, v17, s[24:25]
	s_and_b64 exec, s[2:3], s[24:25]
	v_lshrrev_b32_e32 v92, 15, v27
	v_and_b32_e32 v92, 0x1fffc, v92
	v_add_u32_e32 v92, v18, v92
	ds_add_u32 v92, v100
	s_mov_b64 exec, s[2:3]
	s_waitcnt vmcnt(6)
	v_cndmask_b32_e64 v28, -1, v15, s[26:27]
	s_and_b64 exec, s[2:3], s[26:27]
	v_lshrrev_b32_e32 v93, 15, v28
	v_and_b32_e32 v93, 0x1fffc, v93
	v_add_u32_e32 v93, v18, v93
	ds_add_u32 v93, v100
	s_mov_b64 exec, s[2:3]
	s_waitcnt vmcnt(5)
	v_cndmask_b32_e64 v29, -1, v12, s[28:29]
	s_and_b64 exec, s[2:3], s[28:29]
	v_lshrrev_b32_e32 v94, 15, v29
	v_and_b32_e32 v94, 0x1fffc, v94
	v_add_u32_e32 v94, v18, v94
	ds_add_u32 v94, v100
	s_mov_b64 exec, s[2:3]
	s_waitcnt vmcnt(4)
	v_cndmask_b32_e64 v30, -1, v10, s[30:31]
	s_and_b64 exec, s[2:3], s[30:31]
	v_lshrrev_b32_e32 v95, 15, v30
	v_and_b32_e32 v95, 0x1fffc, v95
	v_add_u32_e32 v95, v18, v95
	ds_add_u32 v95, v100
	s_mov_b64 exec, s[2:3]
	s_waitcnt vmcnt(3)
	v_cndmask_b32_e64 v31, -1, v5, s[34:35]
	s_and_b64 exec, s[2:3], s[34:35]
	v_lshrrev_b32_e32 v96, 15, v31
	v_and_b32_e32 v96, 0x1fffc, v96
	v_add_u32_e32 v96, v18, v96
	ds_add_u32 v96, v100
	s_mov_b64 exec, s[2:3]
	s_waitcnt vmcnt(2)
	v_cndmask_b32_e64 v32, -1, v4, s[36:37]
	s_and_b64 exec, s[2:3], s[36:37]
	v_lshrrev_b32_e32 v97, 15, v32
	v_and_b32_e32 v97, 0x1fffc, v97
	v_add_u32_e32 v97, v18, v97
	ds_add_u32 v97, v100
	s_mov_b64 exec, s[2:3]
	s_waitcnt vmcnt(1)
	v_cndmask_b32_e64 v33, -1, v3, s[6:7]
	s_mov_b64 s[38:39], s[6:7]
	s_and_b64 exec, s[2:3], s[38:39]
	v_lshrrev_b32_e32 v98, 15, v33
	v_and_b32_e32 v98, 0x1fffc, v98
	v_add_u32_e32 v98, v18, v98
	ds_add_u32 v98, v100
	s_mov_b64 exec, s[2:3]
	s_waitcnt vmcnt(0)
	v_cndmask_b32_e32 v34, -1, v2, vcc
	s_mov_b64 s[40:41], vcc
	s_and_b64 exec, s[2:3], s[40:41]
	v_lshrrev_b32_e32 v99, 15, v34
	v_and_b32_e32 v99, 0x1fffc, v99
	v_add_u32_e32 v99, v18, v99
	ds_add_u32 v99, v100
	s_mov_b64 exec, s[2:3]
	s_max_u32 s88, s42, s50
	s_max_u32 s88, s88, s48
	s_max_u32 s88, s88, s43
	s_max_u32 s88, s88, s51
	s_max_u32 s88, s88, s49
	s_max_u32 s88, s88, s66
	s_max_u32 s88, s88, s65
	s_max_u32 s88, s88, s68
	s_max_u32 s88, s88, s67
	s_max_u32 s88, s88, s70
	s_max_u32 s88, s88, s69
	s_max_u32 s88, s88, s72
	s_max_u32 s88, s88, s71
	s_max_u32 s88, s88, s74
	s_max_u32 s88, s88, s73
	s_cmp_gt_u32 s88, 64
	s_mov_b32 s89, s42
	s_mov_b32 s90, s43
	s_cselect_b64 s[42:43], -1, 0
	v_cmp_lt_u32_e64 s[42:43], 64, v3
	s_and_b64 vcc, exec, s[42:43]
	s_cbranch_vccz .LBB2_99
	v_lshlrev_b32_e32 v2, 2, v48
	v_add_u32_e32 v7, 0x17450, v2
	v_or_b32_e32 v4, 64, v45
	v_add_u32_e32 v5, 0x17850, v2
	s_cmp_le_u32 s89, 64
	s_cbranch_scc1 .LBB2_53
	ds_read_b32 v8, v7
	s_waitcnt lgkmcnt(0)
	v_cmp_lt_u32_e32 vcc, v4, v8
	s_and_saveexec_b64 s[2:3], vcc
	s_cbranch_execz .LBB2_53
	ds_read_b32 v9, v5
	s_mov_b64 s[6:7], 0
	v_mov_b32_e32 v3, 0
	v_mov_b32_e32 v10, 1
	v_mov_b32_e32 v11, v4

.LBB2_53:
	s_or_b64 exec, exec, s[2:3]
	s_cmp_le_u32 s50, 64
	s_cbranch_scc1 .LBB2_56
	ds_read_b32 v8, v7 offset:4
	s_waitcnt lgkmcnt(0)
	v_cmp_lt_u32_e32 vcc, v4, v8
	s_and_saveexec_b64 s[2:3], vcc
	s_cbranch_execz .LBB2_56
	ds_read_b32 v9, v5 offset:4
	s_mov_b64 s[6:7], 0
	v_mov_b32_e32 v3, 0
	v_mov_b32_e32 v10, 1
	v_mov_b32_e32 v11, v4

.LBB2_56:
	s_or_b64 exec, exec, s[2:3]
	s_cmp_le_u32 s48, 64
	s_cbranch_scc1 .LBB2_59
	ds_read_b32 v8, v7 offset:8
	s_waitcnt lgkmcnt(0)
	v_cmp_lt_u32_e32 vcc, v4, v8
	s_and_saveexec_b64 s[2:3], vcc
	s_cbranch_execz .LBB2_59
	ds_read_b32 v9, v5 offset:8
	s_mov_b64 s[6:7], 0
	v_mov_b32_e32 v3, 0
	v_mov_b32_e32 v10, 1
	v_mov_b32_e32 v11, v4

.LBB2_59:
	s_or_b64 exec, exec, s[2:3]
	s_cmp_le_u32 s90, 64
	s_cbranch_scc1 .LBB2_62
	ds_read_b32 v8, v7 offset:12
	s_waitcnt lgkmcnt(0)
	v_cmp_lt_u32_e32 vcc, v4, v8
	s_and_saveexec_b64 s[2:3], vcc
	s_cbranch_execz .LBB2_62
	ds_read_b32 v9, v5 offset:12
	s_mov_b64 s[6:7], 0
	v_mov_b32_e32 v3, 0
	v_mov_b32_e32 v10, 1
	v_mov_b32_e32 v11, v4

.LBB2_62:
	s_or_b64 exec, exec, s[2:3]
	s_cmp_le_u32 s51, 64
	s_cbranch_scc1 .LBB2_65
	ds_read_b32 v8, v7 offset:16
	s_waitcnt lgkmcnt(0)
	v_cmp_lt_u32_e32 vcc, v4, v8
	s_and_saveexec_b64 s[2:3], vcc
	s_cbranch_execz .LBB2_65
	ds_read_b32 v9, v5 offset:16
	s_mov_b64 s[6:7], 0
	v_mov_b32_e32 v3, 0
	v_mov_b32_e32 v10, 1
	v_mov_b32_e32 v11, v4

.LBB2_65:
	s_or_b64 exec, exec, s[2:3]
	s_cmp_le_u32 s49, 64
	s_cbranch_scc1 .LBB2_68
	ds_read_b32 v8, v7 offset:20
	s_waitcnt lgkmcnt(0)
	v_cmp_lt_u32_e32 vcc, v4, v8
	s_and_saveexec_b64 s[2:3], vcc
	s_cbranch_execz .LBB2_68
	ds_read_b32 v9, v5 offset:20
	s_mov_b64 s[6:7], 0
	v_mov_b32_e32 v3, 0
	v_mov_b32_e32 v10, 1
	v_mov_b32_e32 v11, v4

.LBB2_68:
	s_or_b64 exec, exec, s[2:3]
	s_cmp_le_u32 s66, 64
	s_cbranch_scc1 .LBB2_71
	ds_read_b32 v8, v7 offset:24
	s_waitcnt lgkmcnt(0)
	v_cmp_lt_u32_e32 vcc, v4, v8
	s_and_saveexec_b64 s[2:3], vcc
	s_cbranch_execz .LBB2_71
	ds_read_b32 v9, v5 offset:24
	s_mov_b64 s[6:7], 0
	v_mov_b32_e32 v3, 0
	v_mov_b32_e32 v10, 1
	v_mov_b32_e32 v11, v4

.LBB2_71:
	s_or_b64 exec, exec, s[2:3]
	s_cmp_le_u32 s65, 64
	s_cbranch_scc1 .LBB2_74
	ds_read_b32 v8, v7 offset:28
	s_waitcnt lgkmcnt(0)
	v_cmp_lt_u32_e32 vcc, v4, v8
	s_and_saveexec_b64 s[2:3], vcc
	s_cbranch_execz .LBB2_74
	ds_read_b32 v9, v5 offset:28
	s_mov_b64 s[6:7], 0
	v_mov_b32_e32 v3, 0
	v_mov_b32_e32 v10, 1
	v_mov_b32_e32 v11, v4

.LBB2_74:
	s_or_b64 exec, exec, s[2:3]
	s_cmp_le_u32 s68, 64
	s_cbranch_scc1 .LBB2_77
	ds_read_b32 v8, v7 offset:32
	s_waitcnt lgkmcnt(0)
	v_cmp_lt_u32_e32 vcc, v4, v8
	s_and_saveexec_b64 s[2:3], vcc
	s_cbranch_execz .LBB2_77
	ds_read_b32 v9, v5 offset:32
	s_mov_b64 s[6:7], 0
	v_mov_b32_e32 v3, 0
	v_mov_b32_e32 v10, 1
	v_mov_b32_e32 v11, v4

.LBB2_77:
	s_or_b64 exec, exec, s[2:3]
	s_cmp_le_u32 s67, 64
	s_cbranch_scc1 .LBB2_80
	ds_read_b32 v8, v7 offset:36
	s_waitcnt lgkmcnt(0)
	v_cmp_lt_u32_e32 vcc, v4, v8
	s_and_saveexec_b64 s[2:3], vcc
	s_cbranch_execz .LBB2_80
	ds_read_b32 v9, v5 offset:36
	s_mov_b64 s[6:7], 0
	v_mov_b32_e32 v3, 0
	v_mov_b32_e32 v10, 1
	v_mov_b32_e32 v11, v4

.LBB2_80:
	s_or_b64 exec, exec, s[2:3]
	s_cmp_le_u32 s70, 64
	s_cbranch_scc1 .LBB2_83
	ds_read_b32 v8, v7 offset:40
	s_waitcnt lgkmcnt(0)
	v_cmp_lt_u32_e32 vcc, v4, v8
	s_and_saveexec_b64 s[2:3], vcc
	s_cbranch_execz .LBB2_83
	ds_read_b32 v9, v5 offset:40
	s_mov_b64 s[6:7], 0
	v_mov_b32_e32 v3, 0
	v_mov_b32_e32 v10, 1
	v_mov_b32_e32 v11, v4

.LBB2_83:
	s_or_b64 exec, exec, s[2:3]
	s_cmp_le_u32 s69, 64
	s_cbranch_scc1 .LBB2_86
	ds_read_b32 v8, v7 offset:44
	s_waitcnt lgkmcnt(0)
	v_cmp_lt_u32_e32 vcc, v4, v8
	s_and_saveexec_b64 s[2:3], vcc
	s_cbranch_execz .LBB2_86
	ds_read_b32 v9, v5 offset:44
	s_mov_b64 s[6:7], 0
	v_mov_b32_e32 v3, 0
	v_mov_b32_e32 v10, 1
	v_mov_b32_e32 v11, v4

.LBB2_86:
	s_or_b64 exec, exec, s[2:3]
	s_cmp_le_u32 s72, 64
	s_cbranch_scc1 .LBB2_89
	ds_read_b32 v8, v7 offset:48
	s_waitcnt lgkmcnt(0)
	v_cmp_lt_u32_e32 vcc, v4, v8
	s_and_saveexec_b64 s[2:3], vcc
	s_cbranch_execz .LBB2_89
	ds_read_b32 v9, v5 offset:48
	s_mov_b64 s[6:7], 0
	v_mov_b32_e32 v3, 0
	v_mov_b32_e32 v10, 1
	v_mov_b32_e32 v11, v4

.LBB2_89:
	s_or_b64 exec, exec, s[2:3]
	s_cmp_le_u32 s71, 64
	s_cbranch_scc1 .LBB2_92
	ds_read_b32 v8, v7 offset:52
	s_waitcnt lgkmcnt(0)
	v_cmp_lt_u32_e32 vcc, v4, v8
	s_and_saveexec_b64 s[2:3], vcc
	s_cbranch_execz .LBB2_92
	ds_read_b32 v9, v5 offset:52
	s_mov_b64 s[6:7], 0
	v_mov_b32_e32 v3, 0
	v_mov_b32_e32 v10, 1
	v_mov_b32_e32 v11, v4

.LBB2_92:
	s_or_b64 exec, exec, s[2:3]
	s_cmp_le_u32 s74, 64
	s_cbranch_scc1 .LBB2_95
	ds_read_b32 v8, v7 offset:56
	s_waitcnt lgkmcnt(0)
	v_cmp_lt_u32_e32 vcc, v4, v8
	s_and_saveexec_b64 s[2:3], vcc
	s_cbranch_execz .LBB2_95
	ds_read_b32 v9, v5 offset:56
	s_mov_b64 s[6:7], 0
	v_mov_b32_e32 v3, 0
	v_mov_b32_e32 v10, 1
	v_mov_b32_e32 v11, v4

.LBB2_95:
	s_or_b64 exec, exec, s[2:3]
	s_cmp_le_u32 s73, 64
	s_cbranch_scc1 .LBB2_98
	ds_read_b32 v7, v7 offset:60
	s_waitcnt lgkmcnt(0)
	v_cmp_lt_u32_e32 vcc, v4, v7
	s_and_saveexec_b64 s[2:3], vcc
	s_cbranch_execz .LBB2_98
	ds_read_b32 v5, v5 offset:60
	s_mov_b64 s[6:7], 0
	v_mov_b32_e32 v3, 0
	v_mov_b32_e32 v8, 1

.LBB2_171:
	v_lshlrev_b32_e32 v2, 2, v48
	v_add_u32_e32 v5, 0x17450, v2
	v_add_u32_e32 v4, 0x17850, v2
	s_cmp_le_u32 s89, 64
	s_cbranch_scc1 .LBB2_176
	ds_read_b32 v3, v5
	s_waitcnt lgkmcnt(0)
	v_readfirstlane_b32 s8, v3
	s_cmpk_lt_u32 s8, 0x41
	s_cbranch_scc1 .LBB2_176
	ds_read_b32 v2, v4
	s_mov_b32 s9, 64
	v_mov_b32_e32 v3, 0
	v_mov_b32_e32 v7, 1
	s_waitcnt lgkmcnt(0)
	v_add_u32_e32 v6, v2, v45
	s_branch .LBB2_174

.LBB2_176:
	s_cmp_le_u32 s50, 64
	s_cbranch_scc1 .LBB2_181
	ds_read_b32 v2, v5 offset:4
	s_waitcnt lgkmcnt(0)
	v_readfirstlane_b32 s8, v2
	s_cmpk_lt_u32 s8, 0x41
	s_cbranch_scc1 .LBB2_181
	ds_read_b32 v2, v4 offset:4
	s_mov_b32 s9, 64
	v_mov_b32_e32 v3, 0
	v_mov_b32_e32 v7, 1
	s_waitcnt lgkmcnt(0)
	v_add_u32_e32 v6, v2, v45
	s_branch .LBB2_179

.LBB2_181:
	s_cmp_le_u32 s48, 64
	s_cbranch_scc1 .LBB2_186
	ds_read_b32 v2, v5 offset:8
	s_waitcnt lgkmcnt(0)
	v_readfirstlane_b32 s8, v2
	s_cmpk_lt_u32 s8, 0x41
	s_cbranch_scc1 .LBB2_186
	ds_read_b32 v2, v4 offset:8
	s_mov_b32 s9, 64
	v_mov_b32_e32 v3, 0
	v_mov_b32_e32 v7, 1
	s_waitcnt lgkmcnt(0)
	v_add_u32_e32 v6, v2, v45
	s_branch .LBB2_184

.LBB2_186:
	s_cmp_le_u32 s90, 64
	s_cbranch_scc1 .LBB2_191
	ds_read_b32 v2, v5 offset:12
	s_waitcnt lgkmcnt(0)
	v_readfirstlane_b32 s8, v2
	s_cmpk_lt_u32 s8, 0x41
	s_cbranch_scc1 .LBB2_191
	ds_read_b32 v2, v4 offset:12
	s_mov_b32 s9, 64
	v_mov_b32_e32 v3, 0
	v_mov_b32_e32 v7, 1
	s_waitcnt lgkmcnt(0)
	v_add_u32_e32 v6, v2, v45
	s_branch .LBB2_189

.LBB2_191:
	s_cmp_le_u32 s51, 64
	s_cbranch_scc1 .LBB2_196
	ds_read_b32 v2, v5 offset:16
	s_waitcnt lgkmcnt(0)
	v_readfirstlane_b32 s8, v2
	s_cmpk_lt_u32 s8, 0x41
	s_cbranch_scc1 .LBB2_196
	ds_read_b32 v2, v4 offset:16
	s_mov_b32 s9, 64
	v_mov_b32_e32 v3, 0
	v_mov_b32_e32 v7, 1
	s_waitcnt lgkmcnt(0)
	v_add_u32_e32 v6, v2, v45
	s_branch .LBB2_194

.LBB2_196:
	s_cmp_le_u32 s49, 64
	s_cbranch_scc1 .LBB2_201
	ds_read_b32 v2, v5 offset:20
	s_waitcnt lgkmcnt(0)
	v_readfirstlane_b32 s8, v2
	s_cmpk_lt_u32 s8, 0x41
	s_cbranch_scc1 .LBB2_201
	ds_read_b32 v2, v4 offset:20
	s_mov_b32 s9, 64
	v_mov_b32_e32 v3, 0
	v_mov_b32_e32 v7, 1
	s_waitcnt lgkmcnt(0)
	v_add_u32_e32 v6, v2, v45
	s_branch .LBB2_199

.LBB2_201:
	s_cmp_le_u32 s66, 64
	s_cbranch_scc1 .LBB2_206
	ds_read_b32 v2, v5 offset:24
	s_waitcnt lgkmcnt(0)
	v_readfirstlane_b32 s8, v2
	s_cmpk_lt_u32 s8, 0x41
	s_cbranch_scc1 .LBB2_206
	ds_read_b32 v2, v4 offset:24
	s_mov_b32 s9, 64
	v_mov_b32_e32 v3, 0
	v_mov_b32_e32 v7, 1
	s_waitcnt lgkmcnt(0)
	v_add_u32_e32 v6, v2, v45
	s_branch .LBB2_204

.LBB2_206:
	s_cmp_le_u32 s65, 64
	s_cbranch_scc1 .LBB2_211
	ds_read_b32 v2, v5 offset:28
	s_waitcnt lgkmcnt(0)
	v_readfirstlane_b32 s8, v2
	s_cmpk_lt_u32 s8, 0x41
	s_cbranch_scc1 .LBB2_211
	ds_read_b32 v2, v4 offset:28
	s_mov_b32 s9, 64
	v_mov_b32_e32 v3, 0
	v_mov_b32_e32 v7, 1
	s_waitcnt lgkmcnt(0)
	v_add_u32_e32 v6, v2, v45
	s_branch .LBB2_209

.LBB2_211:
	s_cmp_le_u32 s68, 64
	s_cbranch_scc1 .LBB2_216
	ds_read_b32 v2, v5 offset:32
	s_waitcnt lgkmcnt(0)
	v_readfirstlane_b32 s8, v2
	s_cmpk_lt_u32 s8, 0x41
	s_cbranch_scc1 .LBB2_216
	ds_read_b32 v2, v4 offset:32
	s_mov_b32 s9, 64
	v_mov_b32_e32 v3, 0
	v_mov_b32_e32 v7, 1
	s_waitcnt lgkmcnt(0)
	v_add_u32_e32 v6, v2, v45
	s_branch .LBB2_214

.LBB2_216:
	s_cmp_le_u32 s67, 64
	s_cbranch_scc1 .LBB2_221
	ds_read_b32 v2, v5 offset:36
	s_waitcnt lgkmcnt(0)
	v_readfirstlane_b32 s8, v2
	s_cmpk_lt_u32 s8, 0x41
	s_cbranch_scc1 .LBB2_221
	ds_read_b32 v2, v4 offset:36
	s_mov_b32 s9, 64
	v_mov_b32_e32 v3, 0
	v_mov_b32_e32 v7, 1
	s_waitcnt lgkmcnt(0)
	v_add_u32_e32 v6, v2, v45
	s_branch .LBB2_219

.LBB2_221:
	s_cmp_le_u32 s70, 64
	s_cbranch_scc1 .LBB2_226
	ds_read_b32 v2, v5 offset:40
	s_waitcnt lgkmcnt(0)
	v_readfirstlane_b32 s8, v2
	s_cmpk_lt_u32 s8, 0x41
	s_cbranch_scc1 .LBB2_226
	ds_read_b32 v2, v4 offset:40
	s_mov_b32 s9, 64
	v_mov_b32_e32 v3, 0
	v_mov_b32_e32 v7, 1
	s_waitcnt lgkmcnt(0)
	v_add_u32_e32 v6, v2, v45
	s_branch .LBB2_224

.LBB2_226:
	s_cmp_le_u32 s69, 64
	s_cbranch_scc1 .LBB2_231
	ds_read_b32 v2, v5 offset:44
	s_waitcnt lgkmcnt(0)
	v_readfirstlane_b32 s8, v2
	s_cmpk_lt_u32 s8, 0x41
	s_cbranch_scc1 .LBB2_231
	ds_read_b32 v2, v4 offset:44
	s_mov_b32 s9, 64
	v_mov_b32_e32 v3, 0
	v_mov_b32_e32 v7, 1
	s_waitcnt lgkmcnt(0)
	v_add_u32_e32 v6, v2, v45
	s_branch .LBB2_229

.LBB2_231:
	s_cmp_le_u32 s72, 64
	s_cbranch_scc1 .LBB2_236
	ds_read_b32 v2, v5 offset:48
	s_waitcnt lgkmcnt(0)
	v_readfirstlane_b32 s8, v2
	s_cmpk_lt_u32 s8, 0x41
	s_cbranch_scc1 .LBB2_236
	ds_read_b32 v2, v4 offset:48
	s_mov_b32 s9, 64
	v_mov_b32_e32 v3, 0
	v_mov_b32_e32 v7, 1
	s_waitcnt lgkmcnt(0)
	v_add_u32_e32 v6, v2, v45
	s_branch .LBB2_234

.LBB2_236:
	s_cmp_le_u32 s71, 64
	s_cbranch_scc1 .LBB2_241
	ds_read_b32 v2, v5 offset:52
	s_waitcnt lgkmcnt(0)
	v_readfirstlane_b32 s8, v2
	s_cmpk_lt_u32 s8, 0x41
	s_cbranch_scc1 .LBB2_241
	ds_read_b32 v2, v4 offset:52
	s_mov_b32 s9, 64
	v_mov_b32_e32 v3, 0
	v_mov_b32_e32 v7, 1
	s_waitcnt lgkmcnt(0)
	v_add_u32_e32 v6, v2, v45
	s_branch .LBB2_239

.LBB2_241:
	s_cmp_le_u32 s74, 64
	s_cbranch_scc1 .LBB2_246
	ds_read_b32 v2, v5 offset:56
	s_waitcnt lgkmcnt(0)
	v_readfirstlane_b32 s8, v2
	s_cmpk_lt_u32 s8, 0x41
	s_cbranch_scc1 .LBB2_246
	ds_read_b32 v2, v4 offset:56
	s_mov_b32 s9, 64
	v_mov_b32_e32 v3, 0
	v_mov_b32_e32 v7, 1
	s_waitcnt lgkmcnt(0)
	v_add_u32_e32 v6, v2, v45
	s_branch .LBB2_244

.LBB2_246:
	s_cmp_le_u32 s73, 64
	s_cbranch_scc1 .LBB2_251
	ds_read_b32 v2, v5 offset:60
	s_waitcnt lgkmcnt(0)
	v_readfirstlane_b32 s8, v2
	s_cmpk_lt_u32 s8, 0x41
	s_cbranch_scc1 .LBB2_251
	ds_read_b32 v2, v4 offset:60
	s_mov_b32 s9, 64
	v_mov_b32_e32 v3, 0
	v_mov_b32_e32 v5, 1
	s_waitcnt lgkmcnt(0)
	v_add_u32_e32 v4, v2, v45
	s_branch .LBB2_249
